# V sweep with three 8-row prefetch buffers (third one in registers freed by parking 14 kernel-lifetime VGPRs in the idle Es LDS area during the sweep)
# speedup vs baseline: 1.0047x; 1.0047x over previous
.Lp6_Adone:
	s_waitcnt vmcnt(0)
	v_lshl_add_u32 v210, v178, 2, s85
	s_mov_b32 s26, 0x3e6d3388
	ds_read_b32 v12, v210 offset:0
	ds_read_b32 v13, v210 offset:12288
	ds_read_b32 v14, v210 offset:256
	ds_read_b32 v15, v210 offset:12544
	ds_read_b32 v16, v210 offset:512
	ds_read_b32 v17, v210 offset:12800
	ds_read_b32 v18, v210 offset:768
	ds_read_b32 v19, v210 offset:13056
	ds_read_b32 v20, v210 offset:1024
	ds_read_b32 v21, v210 offset:13312
	ds_read_b32 v22, v210 offset:1280
	ds_read_b32 v23, v210 offset:13568
	ds_read_b32 v24, v210 offset:1536
	ds_read_b32 v25, v210 offset:13824
	ds_read_b32 v26, v210 offset:1792
	ds_read_b32 v27, v210 offset:14080
	s_waitcnt lgkmcnt(14)
	v_fma_f32 v2, |v12|, s26, 1.0
	v_rcp_f32_e32 v2, v2
	v_mov_b32_e32 v160, 0xbf3a00e3
	v_cmp_gt_f32_e32 vcc, 0, v12
	v_fmamk_f32 v160, v2, 0x3f07dc22, v160
	v_fmaak_f32 v160, v2, v160, 0x3f35f0e3
	v_fmaak_f32 v160, v2, v160, 0xbe11a98e
	v_fmaak_f32 v160, v2, v160, 0x3e027906
	v_mul_f32_e32 v2, v2, v160
	v_mul_f32_e32 v160, v12, v12
	v_mul_f32_e32 v160, 0xbf38aa3b, v160
	v_exp_f32_e32 v160, v160
	s_nop 0
	v_mul_f32_e32 v2, v160, v2
	v_mul_f32_e32 v160, v12, v2
	v_fma_f32 v1, -v12, v2, v12
	v_cndmask_b32_e32 v1, v1, v160, vcc
	v_mul_f32_e32 v1, v13, v1
	ds_write_b32 v210, v1 offset:12288
	s_waitcnt lgkmcnt(13)
	v_fma_f32 v2, |v14|, s26, 1.0
	v_rcp_f32_e32 v2, v2
	v_mov_b32_e32 v160, 0xbf3a00e3
	v_cmp_gt_f32_e32 vcc, 0, v14
	v_fmamk_f32 v160, v2, 0x3f07dc22, v160
	v_fmaak_f32 v160, v2, v160, 0x3f35f0e3
	v_fmaak_f32 v160, v2, v160, 0xbe11a98e
	v_fmaak_f32 v160, v2, v160, 0x3e027906
	v_mul_f32_e32 v2, v2, v160
	v_mul_f32_e32 v160, v14, v14
	v_mul_f32_e32 v160, 0xbf38aa3b, v160
	v_exp_f32_e32 v160, v160
	s_nop 0
	v_mul_f32_e32 v2, v160, v2
	v_mul_f32_e32 v160, v14, v2
	v_fma_f32 v1, -v14, v2, v14
	v_cndmask_b32_e32 v1, v1, v160, vcc
	v_mul_f32_e32 v1, v15, v1
	ds_write_b32 v210, v1 offset:12544
	s_waitcnt lgkmcnt(12)
	v_fma_f32 v2, |v16|, s26, 1.0
	v_rcp_f32_e32 v2, v2
	v_mov_b32_e32 v160, 0xbf3a00e3
	v_cmp_gt_f32_e32 vcc, 0, v16
	v_fmamk_f32 v160, v2, 0x3f07dc22, v160
	v_fmaak_f32 v160, v2, v160, 0x3f35f0e3
	v_fmaak_f32 v160, v2, v160, 0xbe11a98e
	v_fmaak_f32 v160, v2, v160, 0x3e027906
	v_mul_f32_e32 v2, v2, v160
	v_mul_f32_e32 v160, v16, v16
	v_mul_f32_e32 v160, 0xbf38aa3b, v160
	v_exp_f32_e32 v160, v160
	s_nop 0
	v_mul_f32_e32 v2, v160, v2
	v_mul_f32_e32 v160, v16, v2
	v_fma_f32 v1, -v16, v2, v16
	v_cndmask_b32_e32 v1, v1, v160, vcc
	v_mul_f32_e32 v1, v17, v1
	ds_write_b32 v210, v1 offset:12800
	s_waitcnt lgkmcnt(11)
	v_fma_f32 v2, |v18|, s26, 1.0
	v_rcp_f32_e32 v2, v2
	v_mov_b32_e32 v160, 0xbf3a00e3
	v_cmp_gt_f32_e32 vcc, 0, v18
	v_fmamk_f32 v160, v2, 0x3f07dc22, v160
	v_fmaak_f32 v160, v2, v160, 0x3f35f0e3
	v_fmaak_f32 v160, v2, v160, 0xbe11a98e
	v_fmaak_f32 v160, v2, v160, 0x3e027906
	v_mul_f32_e32 v2, v2, v160
	v_mul_f32_e32 v160, v18, v18
	v_mul_f32_e32 v160, 0xbf38aa3b, v160
	v_exp_f32_e32 v160, v160
	s_nop 0
	v_mul_f32_e32 v2, v160, v2
	v_mul_f32_e32 v160, v18, v2
	v_fma_f32 v1, -v18, v2, v18
	v_cndmask_b32_e32 v1, v1, v160, vcc
	v_mul_f32_e32 v1, v19, v1
	ds_write_b32 v210, v1 offset:13056
	s_waitcnt lgkmcnt(10)
	v_fma_f32 v2, |v20|, s26, 1.0
	v_rcp_f32_e32 v2, v2
	v_mov_b32_e32 v160, 0xbf3a00e3
	v_cmp_gt_f32_e32 vcc, 0, v20
	v_fmamk_f32 v160, v2, 0x3f07dc22, v160
	v_fmaak_f32 v160, v2, v160, 0x3f35f0e3
	v_fmaak_f32 v160, v2, v160, 0xbe11a98e
	v_fmaak_f32 v160, v2, v160, 0x3e027906
	v_mul_f32_e32 v2, v2, v160
	v_mul_f32_e32 v160, v20, v20
	v_mul_f32_e32 v160, 0xbf38aa3b, v160
	v_exp_f32_e32 v160, v160
	s_nop 0
	v_mul_f32_e32 v2, v160, v2
	v_mul_f32_e32 v160, v20, v2
	v_fma_f32 v1, -v20, v2, v20
	v_cndmask_b32_e32 v1, v1, v160, vcc
	v_mul_f32_e32 v1, v21, v1
	ds_write_b32 v210, v1 offset:13312
	s_waitcnt lgkmcnt(9)
	v_fma_f32 v2, |v22|, s26, 1.0
	v_rcp_f32_e32 v2, v2
	v_mov_b32_e32 v160, 0xbf3a00e3
	v_cmp_gt_f32_e32 vcc, 0, v22
	v_fmamk_f32 v160, v2, 0x3f07dc22, v160
	v_fmaak_f32 v160, v2, v160, 0x3f35f0e3
	v_fmaak_f32 v160, v2, v160, 0xbe11a98e
	v_fmaak_f32 v160, v2, v160, 0x3e027906
	v_mul_f32_e32 v2, v2, v160
	v_mul_f32_e32 v160, v22, v22
	v_mul_f32_e32 v160, 0xbf38aa3b, v160
	v_exp_f32_e32 v160, v160
	s_nop 0
	v_mul_f32_e32 v2, v160, v2
	v_mul_f32_e32 v160, v22, v2
	v_fma_f32 v1, -v22, v2, v22
	v_cndmask_b32_e32 v1, v1, v160, vcc
	v_mul_f32_e32 v1, v23, v1
	ds_write_b32 v210, v1 offset:13568
	s_waitcnt lgkmcnt(8)
	v_fma_f32 v2, |v24|, s26, 1.0
	v_rcp_f32_e32 v2, v2
	v_mov_b32_e32 v160, 0xbf3a00e3
	v_cmp_gt_f32_e32 vcc, 0, v24
	v_fmamk_f32 v160, v2, 0x3f07dc22, v160
	v_fmaak_f32 v160, v2, v160, 0x3f35f0e3
	v_fmaak_f32 v160, v2, v160, 0xbe11a98e
	v_fmaak_f32 v160, v2, v160, 0x3e027906
	v_mul_f32_e32 v2, v2, v160
	v_mul_f32_e32 v160, v24, v24
	v_mul_f32_e32 v160, 0xbf38aa3b, v160
	v_exp_f32_e32 v160, v160
	s_nop 0
	v_mul_f32_e32 v2, v160, v2
	v_mul_f32_e32 v160, v24, v2
	v_fma_f32 v1, -v24, v2, v24
	v_cndmask_b32_e32 v1, v1, v160, vcc
	v_mul_f32_e32 v1, v25, v1
	ds_write_b32 v210, v1 offset:13824
	s_waitcnt lgkmcnt(7)
	v_fma_f32 v2, |v26|, s26, 1.0
	v_rcp_f32_e32 v2, v2
	v_mov_b32_e32 v160, 0xbf3a00e3
	v_cmp_gt_f32_e32 vcc, 0, v26
	v_fmamk_f32 v160, v2, 0x3f07dc22, v160
	v_fmaak_f32 v160, v2, v160, 0x3f35f0e3
	v_fmaak_f32 v160, v2, v160, 0xbe11a98e
	v_fmaak_f32 v160, v2, v160, 0x3e027906
	v_mul_f32_e32 v2, v2, v160
	v_mul_f32_e32 v160, v26, v26
	v_mul_f32_e32 v160, 0xbf38aa3b, v160
	v_exp_f32_e32 v160, v160
	s_nop 0
	v_mul_f32_e32 v2, v160, v2
	v_mul_f32_e32 v160, v26, v2
	v_fma_f32 v1, -v26, v2, v26
	v_cndmask_b32_e32 v1, v1, v160, vcc
	v_mul_f32_e32 v1, v27, v1
	ds_write_b32 v210, v1 offset:14080
	ds_read_b32 v12, v210 offset:2048
	ds_read_b32 v13, v210 offset:14336
	ds_read_b32 v14, v210 offset:2304
	ds_read_b32 v15, v210 offset:14592
	ds_read_b32 v16, v210 offset:2560
	ds_read_b32 v17, v210 offset:14848
	ds_read_b32 v18, v210 offset:2816
	ds_read_b32 v19, v210 offset:15104
	ds_read_b32 v20, v210 offset:3072
	ds_read_b32 v21, v210 offset:15360
	ds_read_b32 v22, v210 offset:3328
	ds_read_b32 v23, v210 offset:15616
	ds_read_b32 v24, v210 offset:3584
	ds_read_b32 v25, v210 offset:15872
	ds_read_b32 v26, v210 offset:3840
	ds_read_b32 v27, v210 offset:16128
	s_waitcnt lgkmcnt(14)
	v_fma_f32 v2, |v12|, s26, 1.0
	v_rcp_f32_e32 v2, v2
	v_mov_b32_e32 v160, 0xbf3a00e3
	v_cmp_gt_f32_e32 vcc, 0, v12
	v_fmamk_f32 v160, v2, 0x3f07dc22, v160
	v_fmaak_f32 v160, v2, v160, 0x3f35f0e3
	v_fmaak_f32 v160, v2, v160, 0xbe11a98e
	v_fmaak_f32 v160, v2, v160, 0x3e027906
	v_mul_f32_e32 v2, v2, v160
	v_mul_f32_e32 v160, v12, v12
	v_mul_f32_e32 v160, 0xbf38aa3b, v160
	v_exp_f32_e32 v160, v160
	s_nop 0
	v_mul_f32_e32 v2, v160, v2
	v_mul_f32_e32 v160, v12, v2
	v_fma_f32 v1, -v12, v2, v12
	v_cndmask_b32_e32 v1, v1, v160, vcc
	v_mul_f32_e32 v1, v13, v1
	ds_write_b32 v210, v1 offset:14336
	s_waitcnt lgkmcnt(13)
	v_fma_f32 v2, |v14|, s26, 1.0
	v_rcp_f32_e32 v2, v2
	v_mov_b32_e32 v160, 0xbf3a00e3
	v_cmp_gt_f32_e32 vcc, 0, v14
	v_fmamk_f32 v160, v2, 0x3f07dc22, v160
	v_fmaak_f32 v160, v2, v160, 0x3f35f0e3
	v_fmaak_f32 v160, v2, v160, 0xbe11a98e
	v_fmaak_f32 v160, v2, v160, 0x3e027906
	v_mul_f32_e32 v2, v2, v160
	v_mul_f32_e32 v160, v14, v14
	v_mul_f32_e32 v160, 0xbf38aa3b, v160
	v_exp_f32_e32 v160, v160
	s_nop 0
	v_mul_f32_e32 v2, v160, v2
	v_mul_f32_e32 v160, v14, v2
	v_fma_f32 v1, -v14, v2, v14
	v_cndmask_b32_e32 v1, v1, v160, vcc
	v_mul_f32_e32 v1, v15, v1
	ds_write_b32 v210, v1 offset:14592
	s_waitcnt lgkmcnt(12)
	v_fma_f32 v2, |v16|, s26, 1.0
	v_rcp_f32_e32 v2, v2
	v_mov_b32_e32 v160, 0xbf3a00e3
	v_cmp_gt_f32_e32 vcc, 0, v16
	v_fmamk_f32 v160, v2, 0x3f07dc22, v160
	v_fmaak_f32 v160, v2, v160, 0x3f35f0e3
	v_fmaak_f32 v160, v2, v160, 0xbe11a98e
	v_fmaak_f32 v160, v2, v160, 0x3e027906
	v_mul_f32_e32 v2, v2, v160
	v_mul_f32_e32 v160, v16, v16
	v_mul_f32_e32 v160, 0xbf38aa3b, v160
	v_exp_f32_e32 v160, v160
	s_nop 0
	v_mul_f32_e32 v2, v160, v2
	v_mul_f32_e32 v160, v16, v2
	v_fma_f32 v1, -v16, v2, v16
	v_cndmask_b32_e32 v1, v1, v160, vcc
	v_mul_f32_e32 v1, v17, v1
	ds_write_b32 v210, v1 offset:14848
	s_waitcnt lgkmcnt(11)
	v_fma_f32 v2, |v18|, s26, 1.0
	v_rcp_f32_e32 v2, v2
	v_mov_b32_e32 v160, 0xbf3a00e3
	v_cmp_gt_f32_e32 vcc, 0, v18
	v_fmamk_f32 v160, v2, 0x3f07dc22, v160
	v_fmaak_f32 v160, v2, v160, 0x3f35f0e3
	v_fmaak_f32 v160, v2, v160, 0xbe11a98e
	v_fmaak_f32 v160, v2, v160, 0x3e027906
	v_mul_f32_e32 v2, v2, v160
	v_mul_f32_e32 v160, v18, v18
	v_mul_f32_e32 v160, 0xbf38aa3b, v160
	v_exp_f32_e32 v160, v160
	s_nop 0
	v_mul_f32_e32 v2, v160, v2
	v_mul_f32_e32 v160, v18, v2
	v_fma_f32 v1, -v18, v2, v18
	v_cndmask_b32_e32 v1, v1, v160, vcc
	v_mul_f32_e32 v1, v19, v1
	ds_write_b32 v210, v1 offset:15104
	s_waitcnt lgkmcnt(10)
	v_fma_f32 v2, |v20|, s26, 1.0
	v_rcp_f32_e32 v2, v2
	v_mov_b32_e32 v160, 0xbf3a00e3
	v_cmp_gt_f32_e32 vcc, 0, v20
	v_fmamk_f32 v160, v2, 0x3f07dc22, v160
	v_fmaak_f32 v160, v2, v160, 0x3f35f0e3
	v_fmaak_f32 v160, v2, v160, 0xbe11a98e
	v_fmaak_f32 v160, v2, v160, 0x3e027906
	v_mul_f32_e32 v2, v2, v160
	v_mul_f32_e32 v160, v20, v20
	v_mul_f32_e32 v160, 0xbf38aa3b, v160
	v_exp_f32_e32 v160, v160
	s_nop 0
	v_mul_f32_e32 v2, v160, v2
	v_mul_f32_e32 v160, v20, v2
	v_fma_f32 v1, -v20, v2, v20
	v_cndmask_b32_e32 v1, v1, v160, vcc
	v_mul_f32_e32 v1, v21, v1
	ds_write_b32 v210, v1 offset:15360
	s_waitcnt lgkmcnt(9)
	v_fma_f32 v2, |v22|, s26, 1.0
	v_rcp_f32_e32 v2, v2
	v_mov_b32_e32 v160, 0xbf3a00e3
	v_cmp_gt_f32_e32 vcc, 0, v22
	v_fmamk_f32 v160, v2, 0x3f07dc22, v160
	v_fmaak_f32 v160, v2, v160, 0x3f35f0e3
	v_fmaak_f32 v160, v2, v160, 0xbe11a98e
	v_fmaak_f32 v160, v2, v160, 0x3e027906
	v_mul_f32_e32 v2, v2, v160
	v_mul_f32_e32 v160, v22, v22
	v_mul_f32_e32 v160, 0xbf38aa3b, v160
	v_exp_f32_e32 v160, v160
	s_nop 0
	v_mul_f32_e32 v2, v160, v2
	v_mul_f32_e32 v160, v22, v2
	v_fma_f32 v1, -v22, v2, v22
	v_cndmask_b32_e32 v1, v1, v160, vcc
	v_mul_f32_e32 v1, v23, v1
	ds_write_b32 v210, v1 offset:15616
	s_waitcnt lgkmcnt(8)
	v_fma_f32 v2, |v24|, s26, 1.0
	v_rcp_f32_e32 v2, v2
	v_mov_b32_e32 v160, 0xbf3a00e3
	v_cmp_gt_f32_e32 vcc, 0, v24
	v_fmamk_f32 v160, v2, 0x3f07dc22, v160
	v_fmaak_f32 v160, v2, v160, 0x3f35f0e3
	v_fmaak_f32 v160, v2, v160, 0xbe11a98e
	v_fmaak_f32 v160, v2, v160, 0x3e027906
	v_mul_f32_e32 v2, v2, v160
	v_mul_f32_e32 v160, v24, v24
	v_mul_f32_e32 v160, 0xbf38aa3b, v160
	v_exp_f32_e32 v160, v160
	s_nop 0
	v_mul_f32_e32 v2, v160, v2
	v_mul_f32_e32 v160, v24, v2
	v_fma_f32 v1, -v24, v2, v24
	v_cndmask_b32_e32 v1, v1, v160, vcc
	v_mul_f32_e32 v1, v25, v1
	ds_write_b32 v210, v1 offset:15872
	s_waitcnt lgkmcnt(7)
	v_fma_f32 v2, |v26|, s26, 1.0
	v_rcp_f32_e32 v2, v2
	v_mov_b32_e32 v160, 0xbf3a00e3
	v_cmp_gt_f32_e32 vcc, 0, v26
	v_fmamk_f32 v160, v2, 0x3f07dc22, v160
	v_fmaak_f32 v160, v2, v160, 0x3f35f0e3
	v_fmaak_f32 v160, v2, v160, 0xbe11a98e
	v_fmaak_f32 v160, v2, v160, 0x3e027906
	v_mul_f32_e32 v2, v2, v160
	v_mul_f32_e32 v160, v26, v26
	v_mul_f32_e32 v160, 0xbf38aa3b, v160
	v_exp_f32_e32 v160, v160
	s_nop 0
	v_mul_f32_e32 v2, v160, v2
	v_mul_f32_e32 v160, v26, v2
	v_fma_f32 v1, -v26, v2, v26
	v_cndmask_b32_e32 v1, v1, v160, vcc
	v_mul_f32_e32 v1, v27, v1
	ds_write_b32 v210, v1 offset:16128
	s_waitcnt lgkmcnt(0)
	v_mov_b32_e32 v184, 0
	v_mov_b32_e32 v185, 0
	v_mov_b64_e32 v[126:127], v[184:185]
	v_mov_b64_e32 v[128:129], v[184:185]
	v_mov_b64_e32 v[130:131], v[184:185]
	v_mov_b64_e32 v[132:133], v[184:185]
	v_mov_b64_e32 v[134:135], v[184:185]
	v_mov_b64_e32 v[136:137], v[184:185]
	v_mov_b64_e32 v[138:139], v[184:185]
	v_mov_b64_e32 v[140:141], v[184:185]
	v_mov_b64_e32 v[110:111], v[184:185]
	v_mov_b64_e32 v[112:113], v[184:185]
	v_mov_b64_e32 v[114:115], v[184:185]
	v_mov_b64_e32 v[116:117], v[184:185]
	v_mov_b64_e32 v[118:119], v[184:185]
	v_mov_b64_e32 v[120:121], v[184:185]
	v_mov_b64_e32 v[122:123], v[184:185]
	v_mov_b64_e32 v[124:125], v[184:185]
	v_mov_b64_e32 v[94:95], v[184:185]
	v_mov_b64_e32 v[96:97], v[184:185]
	v_mov_b64_e32 v[98:99], v[184:185]
	v_mov_b64_e32 v[100:101], v[184:185]
	v_mov_b64_e32 v[102:103], v[184:185]
	v_mov_b64_e32 v[104:105], v[184:185]
	v_mov_b64_e32 v[106:107], v[184:185]
	v_mov_b64_e32 v[108:109], v[184:185]
	v_mov_b64_e32 v[78:79], v[184:185]
	v_mov_b64_e32 v[80:81], v[184:185]
	v_mov_b64_e32 v[82:83], v[184:185]
	v_mov_b64_e32 v[86:87], v[184:185]
	v_mov_b64_e32 v[88:89], v[184:185]
	v_mov_b64_e32 v[90:91], v[184:185]
	v_mov_b64_e32 v[92:93], v[184:185]
	v_mov_b64_e32 v[84:85], v[184:185]
	v_mov_b64_e32 v[144:145], v[184:185]
	v_mov_b64_e32 v[146:147], v[184:185]
	v_mov_b64_e32 v[148:149], v[184:185]
	v_mov_b64_e32 v[150:151], v[184:185]
	v_mov_b64_e32 v[152:153], v[184:185]
	v_mov_b64_e32 v[154:155], v[184:185]
	v_mov_b64_e32 v[156:157], v[184:185]
	v_mov_b64_e32 v[158:159], v[184:185]
	v_mov_b64_e32 v[160:161], v[184:185]
	v_mov_b64_e32 v[162:163], v[184:185]
	v_mov_b64_e32 v[164:165], v[184:185]
	v_mov_b64_e32 v[166:167], v[184:185]
	v_mov_b64_e32 v[168:169], v[184:185]
	v_mov_b64_e32 v[170:171], v[184:185]
	v_mov_b64_e32 v[172:173], v[184:185]
	v_mov_b64_e32 v[174:175], v[184:185]
	v_mov_b64_e32 v[224:225], v[184:185]
	v_mov_b64_e32 v[226:227], v[184:185]
	v_mov_b64_e32 v[228:229], v[184:185]
	v_mov_b64_e32 v[230:231], v[184:185]
	v_mov_b64_e32 v[232:233], v[184:185]
	v_mov_b64_e32 v[234:235], v[184:185]
	v_mov_b64_e32 v[236:237], v[184:185]
	v_mov_b64_e32 v[238:239], v[184:185]
	v_mov_b64_e32 v[240:241], v[184:185]
	v_mov_b64_e32 v[242:243], v[184:185]
	v_mov_b64_e32 v[244:245], v[184:185]
	v_mov_b64_e32 v[246:247], v[184:185]
	v_mov_b64_e32 v[248:249], v[184:185]
	v_mov_b64_e32 v[250:251], v[184:185]
	v_mov_b64_e32 v[216:217], v[184:185]
	v_mov_b64_e32 v[218:219], v[184:185]
	v_lshl_add_u32 v1, v178, 2, s85
	ds_write_b32 v1, v197 offset:0
	ds_write_b32 v1, v198 offset:256
	ds_write_b32 v1, v199 offset:512
	ds_write_b32 v1, v200 offset:768
	ds_write_b32 v1, v202 offset:1024
	ds_write_b32 v1, v203 offset:1280
	ds_write_b32 v1, v204 offset:1536
	ds_write_b32 v1, v205 offset:1792
	ds_write_b32 v1, v206 offset:2048
	ds_write_b32 v1, v207 offset:2304
	ds_write_b32 v1, v212 offset:2560
	ds_write_b32 v1, v213 offset:2816
	ds_write_b32 v1, v214 offset:3072
	ds_write_b32 v1, v221 offset:3328
	s_waitcnt lgkmcnt(0)
	s_add_i32 s3, s22, -1
	s_min_i32 s2, s3, 0
	s_max_i32 s2, s2, 0
	s_lshl_b32 s2, s2, 2
	s_add_i32 s2, s85, s2
	v_mov_b32_e32 v1, s2
	ds_read_b32 v1, v1 offset:4864
	s_waitcnt lgkmcnt(0)
	v_readfirstlane_b32 s26, v1
	s_and_b32 s2, s26, 0x3ff
	s_bfe_u32 s3, s26, 0x4000a
	v_cmp_gt_u32_e32 vcc, s3, v182
	s_lshl_b32 s2, s2, 2
	s_add_i32 s2, s2, s85
	v_cndmask_b32_e32 v1, 0, v182, vcc
	v_lshl_add_u32 v1, v1, 2, s2
	ds_read_b32 v1, v1 offset:8192
	s_waitcnt lgkmcnt(0)
	v_lshlrev_b32_e32 v1, 10, v1
	v_and_b32_e32 v1, 0x3fffc00, v1
	s_nop 0
	v_readlane_b32 s44, v1, 0
	v_readlane_b32 s45, v1, 1
	v_readlane_b32 s46, v1, 2
	v_readlane_b32 s47, v1, 3
	v_readlane_b32 s48, v1, 4
	v_readlane_b32 s49, v1, 5
	v_readlane_b32 s50, v1, 6
	v_readlane_b32 s51, v1, 7
	s_nop 4
	buffer_load_dwordx4 v[68:71], v181, s[92:95], s44 offen
	buffer_load_dwordx4 v[64:67], v181, s[92:95], s45 offen
	buffer_load_dwordx4 v[60:63], v181, s[92:95], s46 offen
	buffer_load_dwordx4 v[56:59], v181, s[92:95], s47 offen
	buffer_load_dwordx4 v[48:51], v181, s[92:95], s48 offen
	buffer_load_dwordx4 v[32:35], v181, s[92:95], s49 offen
	buffer_load_dwordx4 v[16:19], v181, s[92:95], s50 offen
	buffer_load_dwordx4 v[12:15], v181, s[92:95], s51 offen
	s_add_i32 s3, s22, -1
	s_min_i32 s2, s3, 1
	s_max_i32 s2, s2, 0
	s_lshl_b32 s2, s2, 2
	s_add_i32 s2, s85, s2
	v_mov_b32_e32 v1, s2
	ds_read_b32 v1, v1 offset:4864
	s_waitcnt lgkmcnt(0)
	v_readfirstlane_b32 s86, v1
	s_and_b32 s2, s86, 0x3ff
	s_bfe_u32 s3, s86, 0x4000a
	v_cmp_gt_u32_e32 vcc, s3, v182
	s_lshl_b32 s2, s2, 2
	s_add_i32 s2, s2, s85
	v_cndmask_b32_e32 v1, 0, v182, vcc
	v_lshl_add_u32 v1, v1, 2, s2
	ds_read_b32 v1, v1 offset:8192
	s_waitcnt lgkmcnt(0)
	v_lshlrev_b32_e32 v1, 10, v1
	v_and_b32_e32 v1, 0x3fffc00, v1
	s_nop 0
	v_readlane_b32 s44, v1, 0
	v_readlane_b32 s45, v1, 1
	v_readlane_b32 s46, v1, 2
	v_readlane_b32 s47, v1, 3
	v_readlane_b32 s48, v1, 4
	v_readlane_b32 s49, v1, 5
	v_readlane_b32 s50, v1, 6
	v_readlane_b32 s51, v1, 7
	s_nop 4
	buffer_load_dwordx4 v[72:75], v181, s[92:95], s44 offen
	buffer_load_dwordx4 v[52:55], v181, s[92:95], s45 offen
	buffer_load_dwordx4 v[44:47], v181, s[92:95], s46 offen
	buffer_load_dwordx4 v[40:43], v181, s[92:95], s47 offen
	buffer_load_dwordx4 v[36:39], v181, s[92:95], s48 offen
	buffer_load_dwordx4 v[28:31], v181, s[92:95], s49 offen
	buffer_load_dwordx4 v[24:27], v181, s[92:95], s50 offen
	buffer_load_dwordx4 v[20:23], v181, s[92:95], s51 offen
	s_add_i32 s3, s22, -1
	s_min_i32 s2, s3, 2
	s_max_i32 s2, s2, 0
	s_lshl_b32 s2, s2, 2
	s_add_i32 s2, s85, s2
	v_mov_b32_e32 v1, s2
	ds_read_b32 v1, v1 offset:4864
	s_waitcnt lgkmcnt(0)
	v_readfirstlane_b32 s27, v1
	s_and_b32 s2, s27, 0x3ff
	s_bfe_u32 s3, s27, 0x4000a
	v_cmp_gt_u32_e32 vcc, s3, v182
	s_lshl_b32 s2, s2, 2
	s_add_i32 s2, s2, s85
	v_cndmask_b32_e32 v1, 0, v182, vcc
	v_lshl_add_u32 v1, v1, 2, s2
	ds_read_b32 v1, v1 offset:8192
	s_waitcnt lgkmcnt(0)
	v_lshlrev_b32_e32 v1, 10, v1
	v_and_b32_e32 v1, 0x3fffc00, v1
	s_nop 0
	v_readlane_b32 s44, v1, 0
	v_readlane_b32 s45, v1, 1
	v_readlane_b32 s46, v1, 2
	v_readlane_b32 s47, v1, 3
	v_readlane_b32 s48, v1, 4
	v_readlane_b32 s49, v1, 5
	v_readlane_b32 s50, v1, 6
	v_readlane_b32 s51, v1, 7
	s_nop 4
	buffer_load_dwordx4 v[4:7], v181, s[92:95], s44 offen
	buffer_load_dwordx4 v[8:11], v181, s[92:95], s45 offen
	buffer_load_dwordx4 v[192:195], v181, s[92:95], s46 offen
	buffer_load_dwordx4 v[196:199], v181, s[92:95], s47 offen
	buffer_load_dwordx4 v[200:203], v181, s[92:95], s48 offen
	buffer_load_dwordx4 v[204:207], v181, s[92:95], s49 offen
	buffer_load_dwordx4 v[212:215], v181, s[92:95], s50 offen
	buffer_load_dwordx4 v[220:223], v181, s[92:95], s51 offen
	s_add_i32 s3, s22, -1
	s_min_i32 s2, s3, 3
	s_max_i32 s2, s2, 0
	s_lshl_b32 s2, s2, 2
	s_add_i32 s2, s85, s2
	v_mov_b32_e32 v1, s2
	ds_read_b32 v1, v1 offset:4864
	s_waitcnt lgkmcnt(0)
	v_readfirstlane_b32 s32, v1
	s_mov_b32 s23, 0
.Lp6c0_top:
	s_add_i32 s23, s23, 1
	s_add_i32 s2, s23, 3
	s_add_i32 s3, s22, -1
	s_min_i32 s2, s2, s3
	s_lshl_b32 s2, s2, 2
	s_add_i32 s2, s85, s2
	v_mov_b32_e32 v1, s2
	ds_read_b32 v252, v1 offset:4864
	s_and_b32 s2, s32, 0x3ff
	s_bfe_u32 s3, s32, 0x4000a
	v_cmp_gt_u32_e32 vcc, s3, v182
	s_lshl_b32 s2, s2, 2
	s_add_i32 s2, s2, s85
	v_cndmask_b32_e32 v1, 0, v182, vcc
	v_lshl_add_u32 v1, v1, 2, s2
	ds_read_b32 v1, v1 offset:8192
	s_bfe_u32 s14, s26, 0x4000a
	v_cmp_gt_u32_e32 vcc, s14, v180
	v_mov_b32_e32 v2, 0
	s_and_b32 s2, s26, 0x3ff
	s_lshr_b32 s66, s26, 14
	s_and_saveexec_b64 s[14:15], vcc
	v_add_u32_e32 v210, s2, v180
	v_lshl_add_u32 v210, v210, 2, s85
	ds_read_b32 v2, v210 offset:12288
	s_or_b64 exec, exec, s[14:15]
	s_waitcnt vmcnt(16)
	s_waitcnt lgkmcnt(0)
	v_readfirstlane_b32 s37, v252
	v_lshlrev_b32_e32 v1, 10, v1
	v_and_b32_e32 v1, 0x3fffc00, v1
	s_nop 0
	v_readlane_b32 s44, v1, 0
	v_readlane_b32 s45, v1, 1
	v_readlane_b32 s46, v1, 2
	v_readlane_b32 s47, v1, 3
	v_readlane_b32 s48, v1, 4
	v_readlane_b32 s49, v1, 5
	v_readlane_b32 s50, v1, 6
	v_readlane_b32 s51, v1, 7
	v_mov_b32_e32 v1, v2
	s_bfe_u32 s36, s26, 0x4000a
	s_cmp_eq_u32 s66, 0
	s_cbranch_scc1 .Lp6c0_t0
	s_cmp_eq_u32 s66, 1
	s_cbranch_scc1 .Lp6c0_t1
	s_cmp_eq_u32 s66, 2
	s_cbranch_scc1 .Lp6c0_t2
	s_cmp_eq_u32 s66, 3
	s_cbranch_scc1 .Lp6c0_t3
	s_cmp_eq_u32 s66, 4
	s_cbranch_scc1 .Lp6c0_t4
	s_cmp_eq_u32 s66, 5
	s_cbranch_scc1 .Lp6c0_t5
	s_cmp_eq_u32 s66, 6
	s_cbranch_scc1 .Lp6c0_t6
	s_branch .Lp6c0_t7

.Lp6c2_t0:
	v_readlane_b32 s14, v1, 0
	v_cvt_pk_f32_fp8_e32 v[184:185], v4
	v_cvt_pk_f32_fp8_sdwa v[186:187], v4 src0_sel:WORD_1
	v_pk_fma_f32 v[126:127], v[184:185], s[14:15], v[126:127] op_sel_hi:[1,0,1]
	v_pk_fma_f32 v[128:129], v[186:187], s[14:15], v[128:129] op_sel_hi:[1,0,1]
	v_cvt_pk_f32_fp8_e32 v[188:189], v5
	v_cvt_pk_f32_fp8_sdwa v[190:191], v5 src0_sel:WORD_1
	v_pk_fma_f32 v[130:131], v[188:189], s[14:15], v[130:131] op_sel_hi:[1,0,1]
	v_pk_fma_f32 v[132:133], v[190:191], s[14:15], v[132:133] op_sel_hi:[1,0,1]
	v_cvt_pk_f32_fp8_e32 v[184:185], v6
	v_cvt_pk_f32_fp8_sdwa v[186:187], v6 src0_sel:WORD_1
	v_pk_fma_f32 v[134:135], v[184:185], s[14:15], v[134:135] op_sel_hi:[1,0,1]
	v_pk_fma_f32 v[136:137], v[186:187], s[14:15], v[136:137] op_sel_hi:[1,0,1]
	v_cvt_pk_f32_fp8_e32 v[188:189], v7
	v_cvt_pk_f32_fp8_sdwa v[190:191], v7 src0_sel:WORD_1
	v_pk_fma_f32 v[138:139], v[188:189], s[14:15], v[138:139] op_sel_hi:[1,0,1]
	v_pk_fma_f32 v[140:141], v[190:191], s[14:15], v[140:141] op_sel_hi:[1,0,1]
	v_readlane_b32 s14, v1, 8
	v_cvt_pk_f32_fp8_e32 v[184:185], v8
	v_cvt_pk_f32_fp8_sdwa v[186:187], v8 src0_sel:WORD_1
	v_pk_fma_f32 v[126:127], v[184:185], s[14:15], v[126:127] op_sel_hi:[1,0,1]
	v_pk_fma_f32 v[128:129], v[186:187], s[14:15], v[128:129] op_sel_hi:[1,0,1]
	v_cvt_pk_f32_fp8_e32 v[188:189], v9
	v_cvt_pk_f32_fp8_sdwa v[190:191], v9 src0_sel:WORD_1
	v_pk_fma_f32 v[130:131], v[188:189], s[14:15], v[130:131] op_sel_hi:[1,0,1]
	v_pk_fma_f32 v[132:133], v[190:191], s[14:15], v[132:133] op_sel_hi:[1,0,1]
	v_cvt_pk_f32_fp8_e32 v[184:185], v10
	v_cvt_pk_f32_fp8_sdwa v[186:187], v10 src0_sel:WORD_1
	v_pk_fma_f32 v[134:135], v[184:185], s[14:15], v[134:135] op_sel_hi:[1,0,1]
	v_pk_fma_f32 v[136:137], v[186:187], s[14:15], v[136:137] op_sel_hi:[1,0,1]
	v_cvt_pk_f32_fp8_e32 v[188:189], v11
	v_cvt_pk_f32_fp8_sdwa v[190:191], v11 src0_sel:WORD_1
	v_pk_fma_f32 v[138:139], v[188:189], s[14:15], v[138:139] op_sel_hi:[1,0,1]
	v_pk_fma_f32 v[140:141], v[190:191], s[14:15], v[140:141] op_sel_hi:[1,0,1]
	v_readlane_b32 s14, v1, 16
	v_cvt_pk_f32_fp8_e32 v[184:185], v192
	v_cvt_pk_f32_fp8_sdwa v[186:187], v192 src0_sel:WORD_1
	v_pk_fma_f32 v[126:127], v[184:185], s[14:15], v[126:127] op_sel_hi:[1,0,1]
	v_pk_fma_f32 v[128:129], v[186:187], s[14:15], v[128:129] op_sel_hi:[1,0,1]
	v_cvt_pk_f32_fp8_e32 v[188:189], v193
	v_cvt_pk_f32_fp8_sdwa v[190:191], v193 src0_sel:WORD_1
	v_pk_fma_f32 v[130:131], v[188:189], s[14:15], v[130:131] op_sel_hi:[1,0,1]
	v_pk_fma_f32 v[132:133], v[190:191], s[14:15], v[132:133] op_sel_hi:[1,0,1]
	v_cvt_pk_f32_fp8_e32 v[184:185], v194
	v_cvt_pk_f32_fp8_sdwa v[186:187], v194 src0_sel:WORD_1
	v_pk_fma_f32 v[134:135], v[184:185], s[14:15], v[134:135] op_sel_hi:[1,0,1]
	v_pk_fma_f32 v[136:137], v[186:187], s[14:15], v[136:137] op_sel_hi:[1,0,1]
	v_cvt_pk_f32_fp8_e32 v[188:189], v195
	v_cvt_pk_f32_fp8_sdwa v[190:191], v195 src0_sel:WORD_1
	v_pk_fma_f32 v[138:139], v[188:189], s[14:15], v[138:139] op_sel_hi:[1,0,1]
	v_pk_fma_f32 v[140:141], v[190:191], s[14:15], v[140:141] op_sel_hi:[1,0,1]
	v_readlane_b32 s14, v1, 24
	v_cvt_pk_f32_fp8_e32 v[184:185], v196
	v_cvt_pk_f32_fp8_sdwa v[186:187], v196 src0_sel:WORD_1
	v_pk_fma_f32 v[126:127], v[184:185], s[14:15], v[126:127] op_sel_hi:[1,0,1]
	v_pk_fma_f32 v[128:129], v[186:187], s[14:15], v[128:129] op_sel_hi:[1,0,1]
	v_cvt_pk_f32_fp8_e32 v[188:189], v197
	v_cvt_pk_f32_fp8_sdwa v[190:191], v197 src0_sel:WORD_1
	v_pk_fma_f32 v[130:131], v[188:189], s[14:15], v[130:131] op_sel_hi:[1,0,1]
	v_pk_fma_f32 v[132:133], v[190:191], s[14:15], v[132:133] op_sel_hi:[1,0,1]
	v_cvt_pk_f32_fp8_e32 v[184:185], v198
	v_cvt_pk_f32_fp8_sdwa v[186:187], v198 src0_sel:WORD_1
	v_pk_fma_f32 v[134:135], v[184:185], s[14:15], v[134:135] op_sel_hi:[1,0,1]
	v_pk_fma_f32 v[136:137], v[186:187], s[14:15], v[136:137] op_sel_hi:[1,0,1]
	v_cvt_pk_f32_fp8_e32 v[188:189], v199
	v_cvt_pk_f32_fp8_sdwa v[190:191], v199 src0_sel:WORD_1
	v_pk_fma_f32 v[138:139], v[188:189], s[14:15], v[138:139] op_sel_hi:[1,0,1]
	v_pk_fma_f32 v[140:141], v[190:191], s[14:15], v[140:141] op_sel_hi:[1,0,1]
	v_readlane_b32 s14, v1, 32
	v_cvt_pk_f32_fp8_e32 v[184:185], v200
	v_cvt_pk_f32_fp8_sdwa v[186:187], v200 src0_sel:WORD_1
	v_pk_fma_f32 v[126:127], v[184:185], s[14:15], v[126:127] op_sel_hi:[1,0,1]
	v_pk_fma_f32 v[128:129], v[186:187], s[14:15], v[128:129] op_sel_hi:[1,0,1]
	v_cvt_pk_f32_fp8_e32 v[188:189], v201
	v_cvt_pk_f32_fp8_sdwa v[190:191], v201 src0_sel:WORD_1
	v_pk_fma_f32 v[130:131], v[188:189], s[14:15], v[130:131] op_sel_hi:[1,0,1]
	v_pk_fma_f32 v[132:133], v[190:191], s[14:15], v[132:133] op_sel_hi:[1,0,1]
	v_cvt_pk_f32_fp8_e32 v[184:185], v202
	v_cvt_pk_f32_fp8_sdwa v[186:187], v202 src0_sel:WORD_1
	v_pk_fma_f32 v[134:135], v[184:185], s[14:15], v[134:135] op_sel_hi:[1,0,1]
	v_pk_fma_f32 v[136:137], v[186:187], s[14:15], v[136:137] op_sel_hi:[1,0,1]
	v_cvt_pk_f32_fp8_e32 v[188:189], v203
	v_cvt_pk_f32_fp8_sdwa v[190:191], v203 src0_sel:WORD_1
	v_pk_fma_f32 v[138:139], v[188:189], s[14:15], v[138:139] op_sel_hi:[1,0,1]
	v_pk_fma_f32 v[140:141], v[190:191], s[14:15], v[140:141] op_sel_hi:[1,0,1]
	v_readlane_b32 s14, v1, 40
	v_cvt_pk_f32_fp8_e32 v[184:185], v204
	v_cvt_pk_f32_fp8_sdwa v[186:187], v204 src0_sel:WORD_1
	v_pk_fma_f32 v[126:127], v[184:185], s[14:15], v[126:127] op_sel_hi:[1,0,1]
	v_pk_fma_f32 v[128:129], v[186:187], s[14:15], v[128:129] op_sel_hi:[1,0,1]
	v_cvt_pk_f32_fp8_e32 v[188:189], v205
	v_cvt_pk_f32_fp8_sdwa v[190:191], v205 src0_sel:WORD_1
	v_pk_fma_f32 v[130:131], v[188:189], s[14:15], v[130:131] op_sel_hi:[1,0,1]
	v_pk_fma_f32 v[132:133], v[190:191], s[14:15], v[132:133] op_sel_hi:[1,0,1]
	v_cvt_pk_f32_fp8_e32 v[184:185], v206
	v_cvt_pk_f32_fp8_sdwa v[186:187], v206 src0_sel:WORD_1
	v_pk_fma_f32 v[134:135], v[184:185], s[14:15], v[134:135] op_sel_hi:[1,0,1]
	v_pk_fma_f32 v[136:137], v[186:187], s[14:15], v[136:137] op_sel_hi:[1,0,1]
	v_cvt_pk_f32_fp8_e32 v[188:189], v207
	v_cvt_pk_f32_fp8_sdwa v[190:191], v207 src0_sel:WORD_1
	v_pk_fma_f32 v[138:139], v[188:189], s[14:15], v[138:139] op_sel_hi:[1,0,1]
	v_pk_fma_f32 v[140:141], v[190:191], s[14:15], v[140:141] op_sel_hi:[1,0,1]
	v_readlane_b32 s14, v1, 48
	v_cvt_pk_f32_fp8_e32 v[184:185], v212
	v_cvt_pk_f32_fp8_sdwa v[186:187], v212 src0_sel:WORD_1
	v_pk_fma_f32 v[126:127], v[184:185], s[14:15], v[126:127] op_sel_hi:[1,0,1]
	v_pk_fma_f32 v[128:129], v[186:187], s[14:15], v[128:129] op_sel_hi:[1,0,1]
	v_cvt_pk_f32_fp8_e32 v[188:189], v213
	v_cvt_pk_f32_fp8_sdwa v[190:191], v213 src0_sel:WORD_1
	v_pk_fma_f32 v[130:131], v[188:189], s[14:15], v[130:131] op_sel_hi:[1,0,1]
	v_pk_fma_f32 v[132:133], v[190:191], s[14:15], v[132:133] op_sel_hi:[1,0,1]
	v_cvt_pk_f32_fp8_e32 v[184:185], v214
	v_cvt_pk_f32_fp8_sdwa v[186:187], v214 src0_sel:WORD_1
	v_pk_fma_f32 v[134:135], v[184:185], s[14:15], v[134:135] op_sel_hi:[1,0,1]
	v_pk_fma_f32 v[136:137], v[186:187], s[14:15], v[136:137] op_sel_hi:[1,0,1]
	v_cvt_pk_f32_fp8_e32 v[188:189], v215
	v_cvt_pk_f32_fp8_sdwa v[190:191], v215 src0_sel:WORD_1
	v_pk_fma_f32 v[138:139], v[188:189], s[14:15], v[138:139] op_sel_hi:[1,0,1]
	v_pk_fma_f32 v[140:141], v[190:191], s[14:15], v[140:141] op_sel_hi:[1,0,1]
	v_readlane_b32 s14, v1, 56
	v_cvt_pk_f32_fp8_e32 v[184:185], v220
	v_cvt_pk_f32_fp8_sdwa v[186:187], v220 src0_sel:WORD_1
	v_pk_fma_f32 v[126:127], v[184:185], s[14:15], v[126:127] op_sel_hi:[1,0,1]
	v_pk_fma_f32 v[128:129], v[186:187], s[14:15], v[128:129] op_sel_hi:[1,0,1]
	v_cvt_pk_f32_fp8_e32 v[188:189], v221
	v_cvt_pk_f32_fp8_sdwa v[190:191], v221 src0_sel:WORD_1
	v_pk_fma_f32 v[130:131], v[188:189], s[14:15], v[130:131] op_sel_hi:[1,0,1]
	v_pk_fma_f32 v[132:133], v[190:191], s[14:15], v[132:133] op_sel_hi:[1,0,1]
	v_cvt_pk_f32_fp8_e32 v[184:185], v222
	v_cvt_pk_f32_fp8_sdwa v[186:187], v222 src0_sel:WORD_1
	v_pk_fma_f32 v[134:135], v[184:185], s[14:15], v[134:135] op_sel_hi:[1,0,1]
	v_pk_fma_f32 v[136:137], v[186:187], s[14:15], v[136:137] op_sel_hi:[1,0,1]
	v_cvt_pk_f32_fp8_e32 v[188:189], v223
	v_cvt_pk_f32_fp8_sdwa v[190:191], v223 src0_sel:WORD_1
	v_pk_fma_f32 v[138:139], v[188:189], s[14:15], v[138:139] op_sel_hi:[1,0,1]
	v_pk_fma_f32 v[140:141], v[190:191], s[14:15], v[140:141] op_sel_hi:[1,0,1]
	s_branch .Lp6c2_axdone
.Lp6c2_t1:
	v_readlane_b32 s14, v1, 0
	v_cvt_pk_f32_fp8_e32 v[184:185], v4
	v_cvt_pk_f32_fp8_sdwa v[186:187], v4 src0_sel:WORD_1
	v_pk_fma_f32 v[110:111], v[184:185], s[14:15], v[110:111] op_sel_hi:[1,0,1]
	v_pk_fma_f32 v[112:113], v[186:187], s[14:15], v[112:113] op_sel_hi:[1,0,1]
	v_cvt_pk_f32_fp8_e32 v[188:189], v5
	v_cvt_pk_f32_fp8_sdwa v[190:191], v5 src0_sel:WORD_1
	v_pk_fma_f32 v[114:115], v[188:189], s[14:15], v[114:115] op_sel_hi:[1,0,1]
	v_pk_fma_f32 v[116:117], v[190:191], s[14:15], v[116:117] op_sel_hi:[1,0,1]
	v_cvt_pk_f32_fp8_e32 v[184:185], v6
	v_cvt_pk_f32_fp8_sdwa v[186:187], v6 src0_sel:WORD_1
	v_pk_fma_f32 v[118:119], v[184:185], s[14:15], v[118:119] op_sel_hi:[1,0,1]
	v_pk_fma_f32 v[120:121], v[186:187], s[14:15], v[120:121] op_sel_hi:[1,0,1]
	v_cvt_pk_f32_fp8_e32 v[188:189], v7
	v_cvt_pk_f32_fp8_sdwa v[190:191], v7 src0_sel:WORD_1
	v_pk_fma_f32 v[122:123], v[188:189], s[14:15], v[122:123] op_sel_hi:[1,0,1]
	v_pk_fma_f32 v[124:125], v[190:191], s[14:15], v[124:125] op_sel_hi:[1,0,1]
	v_readlane_b32 s14, v1, 8
	v_cvt_pk_f32_fp8_e32 v[184:185], v8
	v_cvt_pk_f32_fp8_sdwa v[186:187], v8 src0_sel:WORD_1
	v_pk_fma_f32 v[110:111], v[184:185], s[14:15], v[110:111] op_sel_hi:[1,0,1]
	v_pk_fma_f32 v[112:113], v[186:187], s[14:15], v[112:113] op_sel_hi:[1,0,1]
	v_cvt_pk_f32_fp8_e32 v[188:189], v9
	v_cvt_pk_f32_fp8_sdwa v[190:191], v9 src0_sel:WORD_1
	v_pk_fma_f32 v[114:115], v[188:189], s[14:15], v[114:115] op_sel_hi:[1,0,1]
	v_pk_fma_f32 v[116:117], v[190:191], s[14:15], v[116:117] op_sel_hi:[1,0,1]
	v_cvt_pk_f32_fp8_e32 v[184:185], v10
	v_cvt_pk_f32_fp8_sdwa v[186:187], v10 src0_sel:WORD_1
	v_pk_fma_f32 v[118:119], v[184:185], s[14:15], v[118:119] op_sel_hi:[1,0,1]
	v_pk_fma_f32 v[120:121], v[186:187], s[14:15], v[120:121] op_sel_hi:[1,0,1]
	v_cvt_pk_f32_fp8_e32 v[188:189], v11
	v_cvt_pk_f32_fp8_sdwa v[190:191], v11 src0_sel:WORD_1
	v_pk_fma_f32 v[122:123], v[188:189], s[14:15], v[122:123] op_sel_hi:[1,0,1]
	v_pk_fma_f32 v[124:125], v[190:191], s[14:15], v[124:125] op_sel_hi:[1,0,1]
	v_readlane_b32 s14, v1, 16
	v_cvt_pk_f32_fp8_e32 v[184:185], v192
	v_cvt_pk_f32_fp8_sdwa v[186:187], v192 src0_sel:WORD_1
	v_pk_fma_f32 v[110:111], v[184:185], s[14:15], v[110:111] op_sel_hi:[1,0,1]
	v_pk_fma_f32 v[112:113], v[186:187], s[14:15], v[112:113] op_sel_hi:[1,0,1]
	v_cvt_pk_f32_fp8_e32 v[188:189], v193
	v_cvt_pk_f32_fp8_sdwa v[190:191], v193 src0_sel:WORD_1
	v_pk_fma_f32 v[114:115], v[188:189], s[14:15], v[114:115] op_sel_hi:[1,0,1]
	v_pk_fma_f32 v[116:117], v[190:191], s[14:15], v[116:117] op_sel_hi:[1,0,1]
	v_cvt_pk_f32_fp8_e32 v[184:185], v194
	v_cvt_pk_f32_fp8_sdwa v[186:187], v194 src0_sel:WORD_1
	v_pk_fma_f32 v[118:119], v[184:185], s[14:15], v[118:119] op_sel_hi:[1,0,1]
	v_pk_fma_f32 v[120:121], v[186:187], s[14:15], v[120:121] op_sel_hi:[1,0,1]
	v_cvt_pk_f32_fp8_e32 v[188:189], v195
	v_cvt_pk_f32_fp8_sdwa v[190:191], v195 src0_sel:WORD_1
	v_pk_fma_f32 v[122:123], v[188:189], s[14:15], v[122:123] op_sel_hi:[1,0,1]
	v_pk_fma_f32 v[124:125], v[190:191], s[14:15], v[124:125] op_sel_hi:[1,0,1]
	v_readlane_b32 s14, v1, 24
	v_cvt_pk_f32_fp8_e32 v[184:185], v196
	v_cvt_pk_f32_fp8_sdwa v[186:187], v196 src0_sel:WORD_1
	v_pk_fma_f32 v[110:111], v[184:185], s[14:15], v[110:111] op_sel_hi:[1,0,1]
	v_pk_fma_f32 v[112:113], v[186:187], s[14:15], v[112:113] op_sel_hi:[1,0,1]
	v_cvt_pk_f32_fp8_e32 v[188:189], v197
	v_cvt_pk_f32_fp8_sdwa v[190:191], v197 src0_sel:WORD_1
	v_pk_fma_f32 v[114:115], v[188:189], s[14:15], v[114:115] op_sel_hi:[1,0,1]
	v_pk_fma_f32 v[116:117], v[190:191], s[14:15], v[116:117] op_sel_hi:[1,0,1]
	v_cvt_pk_f32_fp8_e32 v[184:185], v198
	v_cvt_pk_f32_fp8_sdwa v[186:187], v198 src0_sel:WORD_1
	v_pk_fma_f32 v[118:119], v[184:185], s[14:15], v[118:119] op_sel_hi:[1,0,1]
	v_pk_fma_f32 v[120:121], v[186:187], s[14:15], v[120:121] op_sel_hi:[1,0,1]
	v_cvt_pk_f32_fp8_e32 v[188:189], v199
	v_cvt_pk_f32_fp8_sdwa v[190:191], v199 src0_sel:WORD_1
	v_pk_fma_f32 v[122:123], v[188:189], s[14:15], v[122:123] op_sel_hi:[1,0,1]
	v_pk_fma_f32 v[124:125], v[190:191], s[14:15], v[124:125] op_sel_hi:[1,0,1]
	v_readlane_b32 s14, v1, 32
	v_cvt_pk_f32_fp8_e32 v[184:185], v200
	v_cvt_pk_f32_fp8_sdwa v[186:187], v200 src0_sel:WORD_1
	v_pk_fma_f32 v[110:111], v[184:185], s[14:15], v[110:111] op_sel_hi:[1,0,1]
	v_pk_fma_f32 v[112:113], v[186:187], s[14:15], v[112:113] op_sel_hi:[1,0,1]
	v_cvt_pk_f32_fp8_e32 v[188:189], v201
	v_cvt_pk_f32_fp8_sdwa v[190:191], v201 src0_sel:WORD_1
	v_pk_fma_f32 v[114:115], v[188:189], s[14:15], v[114:115] op_sel_hi:[1,0,1]
	v_pk_fma_f32 v[116:117], v[190:191], s[14:15], v[116:117] op_sel_hi:[1,0,1]
	v_cvt_pk_f32_fp8_e32 v[184:185], v202
	v_cvt_pk_f32_fp8_sdwa v[186:187], v202 src0_sel:WORD_1
	v_pk_fma_f32 v[118:119], v[184:185], s[14:15], v[118:119] op_sel_hi:[1,0,1]
	v_pk_fma_f32 v[120:121], v[186:187], s[14:15], v[120:121] op_sel_hi:[1,0,1]
	v_cvt_pk_f32_fp8_e32 v[188:189], v203
	v_cvt_pk_f32_fp8_sdwa v[190:191], v203 src0_sel:WORD_1
	v_pk_fma_f32 v[122:123], v[188:189], s[14:15], v[122:123] op_sel_hi:[1,0,1]
	v_pk_fma_f32 v[124:125], v[190:191], s[14:15], v[124:125] op_sel_hi:[1,0,1]
	v_readlane_b32 s14, v1, 40
	v_cvt_pk_f32_fp8_e32 v[184:185], v204
	v_cvt_pk_f32_fp8_sdwa v[186:187], v204 src0_sel:WORD_1
	v_pk_fma_f32 v[110:111], v[184:185], s[14:15], v[110:111] op_sel_hi:[1,0,1]
	v_pk_fma_f32 v[112:113], v[186:187], s[14:15], v[112:113] op_sel_hi:[1,0,1]
	v_cvt_pk_f32_fp8_e32 v[188:189], v205
	v_cvt_pk_f32_fp8_sdwa v[190:191], v205 src0_sel:WORD_1
	v_pk_fma_f32 v[114:115], v[188:189], s[14:15], v[114:115] op_sel_hi:[1,0,1]
	v_pk_fma_f32 v[116:117], v[190:191], s[14:15], v[116:117] op_sel_hi:[1,0,1]
	v_cvt_pk_f32_fp8_e32 v[184:185], v206
	v_cvt_pk_f32_fp8_sdwa v[186:187], v206 src0_sel:WORD_1
	v_pk_fma_f32 v[118:119], v[184:185], s[14:15], v[118:119] op_sel_hi:[1,0,1]
	v_pk_fma_f32 v[120:121], v[186:187], s[14:15], v[120:121] op_sel_hi:[1,0,1]
	v_cvt_pk_f32_fp8_e32 v[188:189], v207
	v_cvt_pk_f32_fp8_sdwa v[190:191], v207 src0_sel:WORD_1
	v_pk_fma_f32 v[122:123], v[188:189], s[14:15], v[122:123] op_sel_hi:[1,0,1]
	v_pk_fma_f32 v[124:125], v[190:191], s[14:15], v[124:125] op_sel_hi:[1,0,1]
	v_readlane_b32 s14, v1, 48
	v_cvt_pk_f32_fp8_e32 v[184:185], v212
	v_cvt_pk_f32_fp8_sdwa v[186:187], v212 src0_sel:WORD_1
	v_pk_fma_f32 v[110:111], v[184:185], s[14:15], v[110:111] op_sel_hi:[1,0,1]
	v_pk_fma_f32 v[112:113], v[186:187], s[14:15], v[112:113] op_sel_hi:[1,0,1]
	v_cvt_pk_f32_fp8_e32 v[188:189], v213
	v_cvt_pk_f32_fp8_sdwa v[190:191], v213 src0_sel:WORD_1
	v_pk_fma_f32 v[114:115], v[188:189], s[14:15], v[114:115] op_sel_hi:[1,0,1]
	v_pk_fma_f32 v[116:117], v[190:191], s[14:15], v[116:117] op_sel_hi:[1,0,1]
	v_cvt_pk_f32_fp8_e32 v[184:185], v214
	v_cvt_pk_f32_fp8_sdwa v[186:187], v214 src0_sel:WORD_1
	v_pk_fma_f32 v[118:119], v[184:185], s[14:15], v[118:119] op_sel_hi:[1,0,1]
	v_pk_fma_f32 v[120:121], v[186:187], s[14:15], v[120:121] op_sel_hi:[1,0,1]
	v_cvt_pk_f32_fp8_e32 v[188:189], v215
	v_cvt_pk_f32_fp8_sdwa v[190:191], v215 src0_sel:WORD_1
	v_pk_fma_f32 v[122:123], v[188:189], s[14:15], v[122:123] op_sel_hi:[1,0,1]
	v_pk_fma_f32 v[124:125], v[190:191], s[14:15], v[124:125] op_sel_hi:[1,0,1]
	v_readlane_b32 s14, v1, 56
	v_cvt_pk_f32_fp8_e32 v[184:185], v220
	v_cvt_pk_f32_fp8_sdwa v[186:187], v220 src0_sel:WORD_1
	v_pk_fma_f32 v[110:111], v[184:185], s[14:15], v[110:111] op_sel_hi:[1,0,1]
	v_pk_fma_f32 v[112:113], v[186:187], s[14:15], v[112:113] op_sel_hi:[1,0,1]
	v_cvt_pk_f32_fp8_e32 v[188:189], v221
	v_cvt_pk_f32_fp8_sdwa v[190:191], v221 src0_sel:WORD_1
	v_pk_fma_f32 v[114:115], v[188:189], s[14:15], v[114:115] op_sel_hi:[1,0,1]
	v_pk_fma_f32 v[116:117], v[190:191], s[14:15], v[116:117] op_sel_hi:[1,0,1]
	v_cvt_pk_f32_fp8_e32 v[184:185], v222
	v_cvt_pk_f32_fp8_sdwa v[186:187], v222 src0_sel:WORD_1
	v_pk_fma_f32 v[118:119], v[184:185], s[14:15], v[118:119] op_sel_hi:[1,0,1]
	v_pk_fma_f32 v[120:121], v[186:187], s[14:15], v[120:121] op_sel_hi:[1,0,1]
	v_cvt_pk_f32_fp8_e32 v[188:189], v223
	v_cvt_pk_f32_fp8_sdwa v[190:191], v223 src0_sel:WORD_1
	v_pk_fma_f32 v[122:123], v[188:189], s[14:15], v[122:123] op_sel_hi:[1,0,1]
	v_pk_fma_f32 v[124:125], v[190:191], s[14:15], v[124:125] op_sel_hi:[1,0,1]
	s_branch .Lp6c2_axdone
.Lp6c2_t2:
	v_readlane_b32 s14, v1, 0
	v_cvt_pk_f32_fp8_e32 v[184:185], v4
	v_cvt_pk_f32_fp8_sdwa v[186:187], v4 src0_sel:WORD_1
	v_pk_fma_f32 v[94:95], v[184:185], s[14:15], v[94:95] op_sel_hi:[1,0,1]
	v_pk_fma_f32 v[96:97], v[186:187], s[14:15], v[96:97] op_sel_hi:[1,0,1]
	v_cvt_pk_f32_fp8_e32 v[188:189], v5
	v_cvt_pk_f32_fp8_sdwa v[190:191], v5 src0_sel:WORD_1
	v_pk_fma_f32 v[98:99], v[188:189], s[14:15], v[98:99] op_sel_hi:[1,0,1]
	v_pk_fma_f32 v[100:101], v[190:191], s[14:15], v[100:101] op_sel_hi:[1,0,1]
	v_cvt_pk_f32_fp8_e32 v[184:185], v6
	v_cvt_pk_f32_fp8_sdwa v[186:187], v6 src0_sel:WORD_1
	v_pk_fma_f32 v[102:103], v[184:185], s[14:15], v[102:103] op_sel_hi:[1,0,1]
	v_pk_fma_f32 v[104:105], v[186:187], s[14:15], v[104:105] op_sel_hi:[1,0,1]
	v_cvt_pk_f32_fp8_e32 v[188:189], v7
	v_cvt_pk_f32_fp8_sdwa v[190:191], v7 src0_sel:WORD_1
	v_pk_fma_f32 v[106:107], v[188:189], s[14:15], v[106:107] op_sel_hi:[1,0,1]
	v_pk_fma_f32 v[108:109], v[190:191], s[14:15], v[108:109] op_sel_hi:[1,0,1]
	v_readlane_b32 s14, v1, 8
	v_cvt_pk_f32_fp8_e32 v[184:185], v8
	v_cvt_pk_f32_fp8_sdwa v[186:187], v8 src0_sel:WORD_1
	v_pk_fma_f32 v[94:95], v[184:185], s[14:15], v[94:95] op_sel_hi:[1,0,1]
	v_pk_fma_f32 v[96:97], v[186:187], s[14:15], v[96:97] op_sel_hi:[1,0,1]
	v_cvt_pk_f32_fp8_e32 v[188:189], v9
	v_cvt_pk_f32_fp8_sdwa v[190:191], v9 src0_sel:WORD_1
	v_pk_fma_f32 v[98:99], v[188:189], s[14:15], v[98:99] op_sel_hi:[1,0,1]
	v_pk_fma_f32 v[100:101], v[190:191], s[14:15], v[100:101] op_sel_hi:[1,0,1]
	v_cvt_pk_f32_fp8_e32 v[184:185], v10
	v_cvt_pk_f32_fp8_sdwa v[186:187], v10 src0_sel:WORD_1
	v_pk_fma_f32 v[102:103], v[184:185], s[14:15], v[102:103] op_sel_hi:[1,0,1]
	v_pk_fma_f32 v[104:105], v[186:187], s[14:15], v[104:105] op_sel_hi:[1,0,1]
	v_cvt_pk_f32_fp8_e32 v[188:189], v11
	v_cvt_pk_f32_fp8_sdwa v[190:191], v11 src0_sel:WORD_1
	v_pk_fma_f32 v[106:107], v[188:189], s[14:15], v[106:107] op_sel_hi:[1,0,1]
	v_pk_fma_f32 v[108:109], v[190:191], s[14:15], v[108:109] op_sel_hi:[1,0,1]
	v_readlane_b32 s14, v1, 16
	v_cvt_pk_f32_fp8_e32 v[184:185], v192
	v_cvt_pk_f32_fp8_sdwa v[186:187], v192 src0_sel:WORD_1
	v_pk_fma_f32 v[94:95], v[184:185], s[14:15], v[94:95] op_sel_hi:[1,0,1]
	v_pk_fma_f32 v[96:97], v[186:187], s[14:15], v[96:97] op_sel_hi:[1,0,1]
	v_cvt_pk_f32_fp8_e32 v[188:189], v193
	v_cvt_pk_f32_fp8_sdwa v[190:191], v193 src0_sel:WORD_1
	v_pk_fma_f32 v[98:99], v[188:189], s[14:15], v[98:99] op_sel_hi:[1,0,1]
	v_pk_fma_f32 v[100:101], v[190:191], s[14:15], v[100:101] op_sel_hi:[1,0,1]
	v_cvt_pk_f32_fp8_e32 v[184:185], v194
	v_cvt_pk_f32_fp8_sdwa v[186:187], v194 src0_sel:WORD_1
	v_pk_fma_f32 v[102:103], v[184:185], s[14:15], v[102:103] op_sel_hi:[1,0,1]
	v_pk_fma_f32 v[104:105], v[186:187], s[14:15], v[104:105] op_sel_hi:[1,0,1]
	v_cvt_pk_f32_fp8_e32 v[188:189], v195
	v_cvt_pk_f32_fp8_sdwa v[190:191], v195 src0_sel:WORD_1
	v_pk_fma_f32 v[106:107], v[188:189], s[14:15], v[106:107] op_sel_hi:[1,0,1]
	v_pk_fma_f32 v[108:109], v[190:191], s[14:15], v[108:109] op_sel_hi:[1,0,1]
	v_readlane_b32 s14, v1, 24
	v_cvt_pk_f32_fp8_e32 v[184:185], v196
	v_cvt_pk_f32_fp8_sdwa v[186:187], v196 src0_sel:WORD_1
	v_pk_fma_f32 v[94:95], v[184:185], s[14:15], v[94:95] op_sel_hi:[1,0,1]
	v_pk_fma_f32 v[96:97], v[186:187], s[14:15], v[96:97] op_sel_hi:[1,0,1]
	v_cvt_pk_f32_fp8_e32 v[188:189], v197
	v_cvt_pk_f32_fp8_sdwa v[190:191], v197 src0_sel:WORD_1
	v_pk_fma_f32 v[98:99], v[188:189], s[14:15], v[98:99] op_sel_hi:[1,0,1]
	v_pk_fma_f32 v[100:101], v[190:191], s[14:15], v[100:101] op_sel_hi:[1,0,1]
	v_cvt_pk_f32_fp8_e32 v[184:185], v198
	v_cvt_pk_f32_fp8_sdwa v[186:187], v198 src0_sel:WORD_1
	v_pk_fma_f32 v[102:103], v[184:185], s[14:15], v[102:103] op_sel_hi:[1,0,1]
	v_pk_fma_f32 v[104:105], v[186:187], s[14:15], v[104:105] op_sel_hi:[1,0,1]
	v_cvt_pk_f32_fp8_e32 v[188:189], v199
	v_cvt_pk_f32_fp8_sdwa v[190:191], v199 src0_sel:WORD_1
	v_pk_fma_f32 v[106:107], v[188:189], s[14:15], v[106:107] op_sel_hi:[1,0,1]
	v_pk_fma_f32 v[108:109], v[190:191], s[14:15], v[108:109] op_sel_hi:[1,0,1]
	v_readlane_b32 s14, v1, 32
	v_cvt_pk_f32_fp8_e32 v[184:185], v200
	v_cvt_pk_f32_fp8_sdwa v[186:187], v200 src0_sel:WORD_1
	v_pk_fma_f32 v[94:95], v[184:185], s[14:15], v[94:95] op_sel_hi:[1,0,1]
	v_pk_fma_f32 v[96:97], v[186:187], s[14:15], v[96:97] op_sel_hi:[1,0,1]
	v_cvt_pk_f32_fp8_e32 v[188:189], v201
	v_cvt_pk_f32_fp8_sdwa v[190:191], v201 src0_sel:WORD_1
	v_pk_fma_f32 v[98:99], v[188:189], s[14:15], v[98:99] op_sel_hi:[1,0,1]
	v_pk_fma_f32 v[100:101], v[190:191], s[14:15], v[100:101] op_sel_hi:[1,0,1]
	v_cvt_pk_f32_fp8_e32 v[184:185], v202
	v_cvt_pk_f32_fp8_sdwa v[186:187], v202 src0_sel:WORD_1
	v_pk_fma_f32 v[102:103], v[184:185], s[14:15], v[102:103] op_sel_hi:[1,0,1]
	v_pk_fma_f32 v[104:105], v[186:187], s[14:15], v[104:105] op_sel_hi:[1,0,1]
	v_cvt_pk_f32_fp8_e32 v[188:189], v203
	v_cvt_pk_f32_fp8_sdwa v[190:191], v203 src0_sel:WORD_1
	v_pk_fma_f32 v[106:107], v[188:189], s[14:15], v[106:107] op_sel_hi:[1,0,1]
	v_pk_fma_f32 v[108:109], v[190:191], s[14:15], v[108:109] op_sel_hi:[1,0,1]
	v_readlane_b32 s14, v1, 40
	v_cvt_pk_f32_fp8_e32 v[184:185], v204
	v_cvt_pk_f32_fp8_sdwa v[186:187], v204 src0_sel:WORD_1
	v_pk_fma_f32 v[94:95], v[184:185], s[14:15], v[94:95] op_sel_hi:[1,0,1]
	v_pk_fma_f32 v[96:97], v[186:187], s[14:15], v[96:97] op_sel_hi:[1,0,1]
	v_cvt_pk_f32_fp8_e32 v[188:189], v205
	v_cvt_pk_f32_fp8_sdwa v[190:191], v205 src0_sel:WORD_1
	v_pk_fma_f32 v[98:99], v[188:189], s[14:15], v[98:99] op_sel_hi:[1,0,1]
	v_pk_fma_f32 v[100:101], v[190:191], s[14:15], v[100:101] op_sel_hi:[1,0,1]
	v_cvt_pk_f32_fp8_e32 v[184:185], v206
	v_cvt_pk_f32_fp8_sdwa v[186:187], v206 src0_sel:WORD_1
	v_pk_fma_f32 v[102:103], v[184:185], s[14:15], v[102:103] op_sel_hi:[1,0,1]
	v_pk_fma_f32 v[104:105], v[186:187], s[14:15], v[104:105] op_sel_hi:[1,0,1]
	v_cvt_pk_f32_fp8_e32 v[188:189], v207
	v_cvt_pk_f32_fp8_sdwa v[190:191], v207 src0_sel:WORD_1
	v_pk_fma_f32 v[106:107], v[188:189], s[14:15], v[106:107] op_sel_hi:[1,0,1]
	v_pk_fma_f32 v[108:109], v[190:191], s[14:15], v[108:109] op_sel_hi:[1,0,1]
	v_readlane_b32 s14, v1, 48
	v_cvt_pk_f32_fp8_e32 v[184:185], v212
	v_cvt_pk_f32_fp8_sdwa v[186:187], v212 src0_sel:WORD_1
	v_pk_fma_f32 v[94:95], v[184:185], s[14:15], v[94:95] op_sel_hi:[1,0,1]
	v_pk_fma_f32 v[96:97], v[186:187], s[14:15], v[96:97] op_sel_hi:[1,0,1]
	v_cvt_pk_f32_fp8_e32 v[188:189], v213
	v_cvt_pk_f32_fp8_sdwa v[190:191], v213 src0_sel:WORD_1
	v_pk_fma_f32 v[98:99], v[188:189], s[14:15], v[98:99] op_sel_hi:[1,0,1]
	v_pk_fma_f32 v[100:101], v[190:191], s[14:15], v[100:101] op_sel_hi:[1,0,1]
	v_cvt_pk_f32_fp8_e32 v[184:185], v214
	v_cvt_pk_f32_fp8_sdwa v[186:187], v214 src0_sel:WORD_1
	v_pk_fma_f32 v[102:103], v[184:185], s[14:15], v[102:103] op_sel_hi:[1,0,1]
	v_pk_fma_f32 v[104:105], v[186:187], s[14:15], v[104:105] op_sel_hi:[1,0,1]
	v_cvt_pk_f32_fp8_e32 v[188:189], v215
	v_cvt_pk_f32_fp8_sdwa v[190:191], v215 src0_sel:WORD_1
	v_pk_fma_f32 v[106:107], v[188:189], s[14:15], v[106:107] op_sel_hi:[1,0,1]
	v_pk_fma_f32 v[108:109], v[190:191], s[14:15], v[108:109] op_sel_hi:[1,0,1]
	v_readlane_b32 s14, v1, 56
	v_cvt_pk_f32_fp8_e32 v[184:185], v220
	v_cvt_pk_f32_fp8_sdwa v[186:187], v220 src0_sel:WORD_1
	v_pk_fma_f32 v[94:95], v[184:185], s[14:15], v[94:95] op_sel_hi:[1,0,1]
	v_pk_fma_f32 v[96:97], v[186:187], s[14:15], v[96:97] op_sel_hi:[1,0,1]
	v_cvt_pk_f32_fp8_e32 v[188:189], v221
	v_cvt_pk_f32_fp8_sdwa v[190:191], v221 src0_sel:WORD_1
	v_pk_fma_f32 v[98:99], v[188:189], s[14:15], v[98:99] op_sel_hi:[1,0,1]
	v_pk_fma_f32 v[100:101], v[190:191], s[14:15], v[100:101] op_sel_hi:[1,0,1]
	v_cvt_pk_f32_fp8_e32 v[184:185], v222
	v_cvt_pk_f32_fp8_sdwa v[186:187], v222 src0_sel:WORD_1
	v_pk_fma_f32 v[102:103], v[184:185], s[14:15], v[102:103] op_sel_hi:[1,0,1]
	v_pk_fma_f32 v[104:105], v[186:187], s[14:15], v[104:105] op_sel_hi:[1,0,1]
	v_cvt_pk_f32_fp8_e32 v[188:189], v223
	v_cvt_pk_f32_fp8_sdwa v[190:191], v223 src0_sel:WORD_1
	v_pk_fma_f32 v[106:107], v[188:189], s[14:15], v[106:107] op_sel_hi:[1,0,1]
	v_pk_fma_f32 v[108:109], v[190:191], s[14:15], v[108:109] op_sel_hi:[1,0,1]
	s_branch .Lp6c2_axdone
.Lp6c2_t3:
	v_readlane_b32 s14, v1, 0
	v_cvt_pk_f32_fp8_e32 v[184:185], v4
	v_cvt_pk_f32_fp8_sdwa v[186:187], v4 src0_sel:WORD_1
	v_pk_fma_f32 v[78:79], v[184:185], s[14:15], v[78:79] op_sel_hi:[1,0,1]
	v_pk_fma_f32 v[80:81], v[186:187], s[14:15], v[80:81] op_sel_hi:[1,0,1]
	v_cvt_pk_f32_fp8_e32 v[188:189], v5
	v_cvt_pk_f32_fp8_sdwa v[190:191], v5 src0_sel:WORD_1
	v_pk_fma_f32 v[82:83], v[188:189], s[14:15], v[82:83] op_sel_hi:[1,0,1]
	v_pk_fma_f32 v[86:87], v[190:191], s[14:15], v[86:87] op_sel_hi:[1,0,1]
	v_cvt_pk_f32_fp8_e32 v[184:185], v6
	v_cvt_pk_f32_fp8_sdwa v[186:187], v6 src0_sel:WORD_1
	v_pk_fma_f32 v[88:89], v[184:185], s[14:15], v[88:89] op_sel_hi:[1,0,1]
	v_pk_fma_f32 v[90:91], v[186:187], s[14:15], v[90:91] op_sel_hi:[1,0,1]
	v_cvt_pk_f32_fp8_e32 v[188:189], v7
	v_cvt_pk_f32_fp8_sdwa v[190:191], v7 src0_sel:WORD_1
	v_pk_fma_f32 v[92:93], v[188:189], s[14:15], v[92:93] op_sel_hi:[1,0,1]
	v_pk_fma_f32 v[84:85], v[190:191], s[14:15], v[84:85] op_sel_hi:[1,0,1]
	v_readlane_b32 s14, v1, 8
	v_cvt_pk_f32_fp8_e32 v[184:185], v8
	v_cvt_pk_f32_fp8_sdwa v[186:187], v8 src0_sel:WORD_1
	v_pk_fma_f32 v[78:79], v[184:185], s[14:15], v[78:79] op_sel_hi:[1,0,1]
	v_pk_fma_f32 v[80:81], v[186:187], s[14:15], v[80:81] op_sel_hi:[1,0,1]
	v_cvt_pk_f32_fp8_e32 v[188:189], v9
	v_cvt_pk_f32_fp8_sdwa v[190:191], v9 src0_sel:WORD_1
	v_pk_fma_f32 v[82:83], v[188:189], s[14:15], v[82:83] op_sel_hi:[1,0,1]
	v_pk_fma_f32 v[86:87], v[190:191], s[14:15], v[86:87] op_sel_hi:[1,0,1]
	v_cvt_pk_f32_fp8_e32 v[184:185], v10
	v_cvt_pk_f32_fp8_sdwa v[186:187], v10 src0_sel:WORD_1
	v_pk_fma_f32 v[88:89], v[184:185], s[14:15], v[88:89] op_sel_hi:[1,0,1]
	v_pk_fma_f32 v[90:91], v[186:187], s[14:15], v[90:91] op_sel_hi:[1,0,1]
	v_cvt_pk_f32_fp8_e32 v[188:189], v11
	v_cvt_pk_f32_fp8_sdwa v[190:191], v11 src0_sel:WORD_1
	v_pk_fma_f32 v[92:93], v[188:189], s[14:15], v[92:93] op_sel_hi:[1,0,1]
	v_pk_fma_f32 v[84:85], v[190:191], s[14:15], v[84:85] op_sel_hi:[1,0,1]
	v_readlane_b32 s14, v1, 16
	v_cvt_pk_f32_fp8_e32 v[184:185], v192
	v_cvt_pk_f32_fp8_sdwa v[186:187], v192 src0_sel:WORD_1
	v_pk_fma_f32 v[78:79], v[184:185], s[14:15], v[78:79] op_sel_hi:[1,0,1]
	v_pk_fma_f32 v[80:81], v[186:187], s[14:15], v[80:81] op_sel_hi:[1,0,1]
	v_cvt_pk_f32_fp8_e32 v[188:189], v193
	v_cvt_pk_f32_fp8_sdwa v[190:191], v193 src0_sel:WORD_1
	v_pk_fma_f32 v[82:83], v[188:189], s[14:15], v[82:83] op_sel_hi:[1,0,1]
	v_pk_fma_f32 v[86:87], v[190:191], s[14:15], v[86:87] op_sel_hi:[1,0,1]
	v_cvt_pk_f32_fp8_e32 v[184:185], v194
	v_cvt_pk_f32_fp8_sdwa v[186:187], v194 src0_sel:WORD_1
	v_pk_fma_f32 v[88:89], v[184:185], s[14:15], v[88:89] op_sel_hi:[1,0,1]
	v_pk_fma_f32 v[90:91], v[186:187], s[14:15], v[90:91] op_sel_hi:[1,0,1]
	v_cvt_pk_f32_fp8_e32 v[188:189], v195
	v_cvt_pk_f32_fp8_sdwa v[190:191], v195 src0_sel:WORD_1
	v_pk_fma_f32 v[92:93], v[188:189], s[14:15], v[92:93] op_sel_hi:[1,0,1]
	v_pk_fma_f32 v[84:85], v[190:191], s[14:15], v[84:85] op_sel_hi:[1,0,1]
	v_readlane_b32 s14, v1, 24
	v_cvt_pk_f32_fp8_e32 v[184:185], v196
	v_cvt_pk_f32_fp8_sdwa v[186:187], v196 src0_sel:WORD_1
	v_pk_fma_f32 v[78:79], v[184:185], s[14:15], v[78:79] op_sel_hi:[1,0,1]
	v_pk_fma_f32 v[80:81], v[186:187], s[14:15], v[80:81] op_sel_hi:[1,0,1]
	v_cvt_pk_f32_fp8_e32 v[188:189], v197
	v_cvt_pk_f32_fp8_sdwa v[190:191], v197 src0_sel:WORD_1
	v_pk_fma_f32 v[82:83], v[188:189], s[14:15], v[82:83] op_sel_hi:[1,0,1]
	v_pk_fma_f32 v[86:87], v[190:191], s[14:15], v[86:87] op_sel_hi:[1,0,1]
	v_cvt_pk_f32_fp8_e32 v[184:185], v198
	v_cvt_pk_f32_fp8_sdwa v[186:187], v198 src0_sel:WORD_1
	v_pk_fma_f32 v[88:89], v[184:185], s[14:15], v[88:89] op_sel_hi:[1,0,1]
	v_pk_fma_f32 v[90:91], v[186:187], s[14:15], v[90:91] op_sel_hi:[1,0,1]
	v_cvt_pk_f32_fp8_e32 v[188:189], v199
	v_cvt_pk_f32_fp8_sdwa v[190:191], v199 src0_sel:WORD_1
	v_pk_fma_f32 v[92:93], v[188:189], s[14:15], v[92:93] op_sel_hi:[1,0,1]
	v_pk_fma_f32 v[84:85], v[190:191], s[14:15], v[84:85] op_sel_hi:[1,0,1]
	v_readlane_b32 s14, v1, 32
	v_cvt_pk_f32_fp8_e32 v[184:185], v200
	v_cvt_pk_f32_fp8_sdwa v[186:187], v200 src0_sel:WORD_1
	v_pk_fma_f32 v[78:79], v[184:185], s[14:15], v[78:79] op_sel_hi:[1,0,1]
	v_pk_fma_f32 v[80:81], v[186:187], s[14:15], v[80:81] op_sel_hi:[1,0,1]
	v_cvt_pk_f32_fp8_e32 v[188:189], v201
	v_cvt_pk_f32_fp8_sdwa v[190:191], v201 src0_sel:WORD_1
	v_pk_fma_f32 v[82:83], v[188:189], s[14:15], v[82:83] op_sel_hi:[1,0,1]
	v_pk_fma_f32 v[86:87], v[190:191], s[14:15], v[86:87] op_sel_hi:[1,0,1]
	v_cvt_pk_f32_fp8_e32 v[184:185], v202
	v_cvt_pk_f32_fp8_sdwa v[186:187], v202 src0_sel:WORD_1
	v_pk_fma_f32 v[88:89], v[184:185], s[14:15], v[88:89] op_sel_hi:[1,0,1]
	v_pk_fma_f32 v[90:91], v[186:187], s[14:15], v[90:91] op_sel_hi:[1,0,1]
	v_cvt_pk_f32_fp8_e32 v[188:189], v203
	v_cvt_pk_f32_fp8_sdwa v[190:191], v203 src0_sel:WORD_1
	v_pk_fma_f32 v[92:93], v[188:189], s[14:15], v[92:93] op_sel_hi:[1,0,1]
	v_pk_fma_f32 v[84:85], v[190:191], s[14:15], v[84:85] op_sel_hi:[1,0,1]
	v_readlane_b32 s14, v1, 40
	v_cvt_pk_f32_fp8_e32 v[184:185], v204
	v_cvt_pk_f32_fp8_sdwa v[186:187], v204 src0_sel:WORD_1
	v_pk_fma_f32 v[78:79], v[184:185], s[14:15], v[78:79] op_sel_hi:[1,0,1]
	v_pk_fma_f32 v[80:81], v[186:187], s[14:15], v[80:81] op_sel_hi:[1,0,1]
	v_cvt_pk_f32_fp8_e32 v[188:189], v205
	v_cvt_pk_f32_fp8_sdwa v[190:191], v205 src0_sel:WORD_1
	v_pk_fma_f32 v[82:83], v[188:189], s[14:15], v[82:83] op_sel_hi:[1,0,1]
	v_pk_fma_f32 v[86:87], v[190:191], s[14:15], v[86:87] op_sel_hi:[1,0,1]
	v_cvt_pk_f32_fp8_e32 v[184:185], v206
	v_cvt_pk_f32_fp8_sdwa v[186:187], v206 src0_sel:WORD_1
	v_pk_fma_f32 v[88:89], v[184:185], s[14:15], v[88:89] op_sel_hi:[1,0,1]
	v_pk_fma_f32 v[90:91], v[186:187], s[14:15], v[90:91] op_sel_hi:[1,0,1]
	v_cvt_pk_f32_fp8_e32 v[188:189], v207
	v_cvt_pk_f32_fp8_sdwa v[190:191], v207 src0_sel:WORD_1
	v_pk_fma_f32 v[92:93], v[188:189], s[14:15], v[92:93] op_sel_hi:[1,0,1]
	v_pk_fma_f32 v[84:85], v[190:191], s[14:15], v[84:85] op_sel_hi:[1,0,1]
	v_readlane_b32 s14, v1, 48
	v_cvt_pk_f32_fp8_e32 v[184:185], v212
	v_cvt_pk_f32_fp8_sdwa v[186:187], v212 src0_sel:WORD_1
	v_pk_fma_f32 v[78:79], v[184:185], s[14:15], v[78:79] op_sel_hi:[1,0,1]
	v_pk_fma_f32 v[80:81], v[186:187], s[14:15], v[80:81] op_sel_hi:[1,0,1]
	v_cvt_pk_f32_fp8_e32 v[188:189], v213
	v_cvt_pk_f32_fp8_sdwa v[190:191], v213 src0_sel:WORD_1
	v_pk_fma_f32 v[82:83], v[188:189], s[14:15], v[82:83] op_sel_hi:[1,0,1]
	v_pk_fma_f32 v[86:87], v[190:191], s[14:15], v[86:87] op_sel_hi:[1,0,1]
	v_cvt_pk_f32_fp8_e32 v[184:185], v214
	v_cvt_pk_f32_fp8_sdwa v[186:187], v214 src0_sel:WORD_1
	v_pk_fma_f32 v[88:89], v[184:185], s[14:15], v[88:89] op_sel_hi:[1,0,1]
	v_pk_fma_f32 v[90:91], v[186:187], s[14:15], v[90:91] op_sel_hi:[1,0,1]
	v_cvt_pk_f32_fp8_e32 v[188:189], v215
	v_cvt_pk_f32_fp8_sdwa v[190:191], v215 src0_sel:WORD_1
	v_pk_fma_f32 v[92:93], v[188:189], s[14:15], v[92:93] op_sel_hi:[1,0,1]
	v_pk_fma_f32 v[84:85], v[190:191], s[14:15], v[84:85] op_sel_hi:[1,0,1]
	v_readlane_b32 s14, v1, 56
	v_cvt_pk_f32_fp8_e32 v[184:185], v220
	v_cvt_pk_f32_fp8_sdwa v[186:187], v220 src0_sel:WORD_1
	v_pk_fma_f32 v[78:79], v[184:185], s[14:15], v[78:79] op_sel_hi:[1,0,1]
	v_pk_fma_f32 v[80:81], v[186:187], s[14:15], v[80:81] op_sel_hi:[1,0,1]
	v_cvt_pk_f32_fp8_e32 v[188:189], v221
	v_cvt_pk_f32_fp8_sdwa v[190:191], v221 src0_sel:WORD_1
	v_pk_fma_f32 v[82:83], v[188:189], s[14:15], v[82:83] op_sel_hi:[1,0,1]
	v_pk_fma_f32 v[86:87], v[190:191], s[14:15], v[86:87] op_sel_hi:[1,0,1]
	v_cvt_pk_f32_fp8_e32 v[184:185], v222
	v_cvt_pk_f32_fp8_sdwa v[186:187], v222 src0_sel:WORD_1
	v_pk_fma_f32 v[88:89], v[184:185], s[14:15], v[88:89] op_sel_hi:[1,0,1]
	v_pk_fma_f32 v[90:91], v[186:187], s[14:15], v[90:91] op_sel_hi:[1,0,1]
	v_cvt_pk_f32_fp8_e32 v[188:189], v223
	v_cvt_pk_f32_fp8_sdwa v[190:191], v223 src0_sel:WORD_1
	v_pk_fma_f32 v[92:93], v[188:189], s[14:15], v[92:93] op_sel_hi:[1,0,1]
	v_pk_fma_f32 v[84:85], v[190:191], s[14:15], v[84:85] op_sel_hi:[1,0,1]
	s_branch .Lp6c2_axdone
.Lp6c2_t4:
	v_readlane_b32 s14, v1, 0
	v_cvt_pk_f32_fp8_e32 v[184:185], v4
	v_cvt_pk_f32_fp8_sdwa v[186:187], v4 src0_sel:WORD_1
	v_pk_fma_f32 v[144:145], v[184:185], s[14:15], v[144:145] op_sel_hi:[1,0,1]
	v_pk_fma_f32 v[146:147], v[186:187], s[14:15], v[146:147] op_sel_hi:[1,0,1]
	v_cvt_pk_f32_fp8_e32 v[188:189], v5
	v_cvt_pk_f32_fp8_sdwa v[190:191], v5 src0_sel:WORD_1
	v_pk_fma_f32 v[148:149], v[188:189], s[14:15], v[148:149] op_sel_hi:[1,0,1]
	v_pk_fma_f32 v[150:151], v[190:191], s[14:15], v[150:151] op_sel_hi:[1,0,1]
	v_cvt_pk_f32_fp8_e32 v[184:185], v6
	v_cvt_pk_f32_fp8_sdwa v[186:187], v6 src0_sel:WORD_1
	v_pk_fma_f32 v[152:153], v[184:185], s[14:15], v[152:153] op_sel_hi:[1,0,1]
	v_pk_fma_f32 v[154:155], v[186:187], s[14:15], v[154:155] op_sel_hi:[1,0,1]
	v_cvt_pk_f32_fp8_e32 v[188:189], v7
	v_cvt_pk_f32_fp8_sdwa v[190:191], v7 src0_sel:WORD_1
	v_pk_fma_f32 v[156:157], v[188:189], s[14:15], v[156:157] op_sel_hi:[1,0,1]
	v_pk_fma_f32 v[158:159], v[190:191], s[14:15], v[158:159] op_sel_hi:[1,0,1]
	v_readlane_b32 s14, v1, 8
	v_cvt_pk_f32_fp8_e32 v[184:185], v8
	v_cvt_pk_f32_fp8_sdwa v[186:187], v8 src0_sel:WORD_1
	v_pk_fma_f32 v[144:145], v[184:185], s[14:15], v[144:145] op_sel_hi:[1,0,1]
	v_pk_fma_f32 v[146:147], v[186:187], s[14:15], v[146:147] op_sel_hi:[1,0,1]
	v_cvt_pk_f32_fp8_e32 v[188:189], v9
	v_cvt_pk_f32_fp8_sdwa v[190:191], v9 src0_sel:WORD_1
	v_pk_fma_f32 v[148:149], v[188:189], s[14:15], v[148:149] op_sel_hi:[1,0,1]
	v_pk_fma_f32 v[150:151], v[190:191], s[14:15], v[150:151] op_sel_hi:[1,0,1]
	v_cvt_pk_f32_fp8_e32 v[184:185], v10
	v_cvt_pk_f32_fp8_sdwa v[186:187], v10 src0_sel:WORD_1
	v_pk_fma_f32 v[152:153], v[184:185], s[14:15], v[152:153] op_sel_hi:[1,0,1]
	v_pk_fma_f32 v[154:155], v[186:187], s[14:15], v[154:155] op_sel_hi:[1,0,1]
	v_cvt_pk_f32_fp8_e32 v[188:189], v11
	v_cvt_pk_f32_fp8_sdwa v[190:191], v11 src0_sel:WORD_1
	v_pk_fma_f32 v[156:157], v[188:189], s[14:15], v[156:157] op_sel_hi:[1,0,1]
	v_pk_fma_f32 v[158:159], v[190:191], s[14:15], v[158:159] op_sel_hi:[1,0,1]
	v_readlane_b32 s14, v1, 16
	v_cvt_pk_f32_fp8_e32 v[184:185], v192
	v_cvt_pk_f32_fp8_sdwa v[186:187], v192 src0_sel:WORD_1
	v_pk_fma_f32 v[144:145], v[184:185], s[14:15], v[144:145] op_sel_hi:[1,0,1]
	v_pk_fma_f32 v[146:147], v[186:187], s[14:15], v[146:147] op_sel_hi:[1,0,1]
	v_cvt_pk_f32_fp8_e32 v[188:189], v193
	v_cvt_pk_f32_fp8_sdwa v[190:191], v193 src0_sel:WORD_1
	v_pk_fma_f32 v[148:149], v[188:189], s[14:15], v[148:149] op_sel_hi:[1,0,1]
	v_pk_fma_f32 v[150:151], v[190:191], s[14:15], v[150:151] op_sel_hi:[1,0,1]
	v_cvt_pk_f32_fp8_e32 v[184:185], v194
	v_cvt_pk_f32_fp8_sdwa v[186:187], v194 src0_sel:WORD_1
	v_pk_fma_f32 v[152:153], v[184:185], s[14:15], v[152:153] op_sel_hi:[1,0,1]
	v_pk_fma_f32 v[154:155], v[186:187], s[14:15], v[154:155] op_sel_hi:[1,0,1]
	v_cvt_pk_f32_fp8_e32 v[188:189], v195
	v_cvt_pk_f32_fp8_sdwa v[190:191], v195 src0_sel:WORD_1
	v_pk_fma_f32 v[156:157], v[188:189], s[14:15], v[156:157] op_sel_hi:[1,0,1]
	v_pk_fma_f32 v[158:159], v[190:191], s[14:15], v[158:159] op_sel_hi:[1,0,1]
	v_readlane_b32 s14, v1, 24
	v_cvt_pk_f32_fp8_e32 v[184:185], v196
	v_cvt_pk_f32_fp8_sdwa v[186:187], v196 src0_sel:WORD_1
	v_pk_fma_f32 v[144:145], v[184:185], s[14:15], v[144:145] op_sel_hi:[1,0,1]
	v_pk_fma_f32 v[146:147], v[186:187], s[14:15], v[146:147] op_sel_hi:[1,0,1]
	v_cvt_pk_f32_fp8_e32 v[188:189], v197
	v_cvt_pk_f32_fp8_sdwa v[190:191], v197 src0_sel:WORD_1
	v_pk_fma_f32 v[148:149], v[188:189], s[14:15], v[148:149] op_sel_hi:[1,0,1]
	v_pk_fma_f32 v[150:151], v[190:191], s[14:15], v[150:151] op_sel_hi:[1,0,1]
	v_cvt_pk_f32_fp8_e32 v[184:185], v198
	v_cvt_pk_f32_fp8_sdwa v[186:187], v198 src0_sel:WORD_1
	v_pk_fma_f32 v[152:153], v[184:185], s[14:15], v[152:153] op_sel_hi:[1,0,1]
	v_pk_fma_f32 v[154:155], v[186:187], s[14:15], v[154:155] op_sel_hi:[1,0,1]
	v_cvt_pk_f32_fp8_e32 v[188:189], v199
	v_cvt_pk_f32_fp8_sdwa v[190:191], v199 src0_sel:WORD_1
	v_pk_fma_f32 v[156:157], v[188:189], s[14:15], v[156:157] op_sel_hi:[1,0,1]
	v_pk_fma_f32 v[158:159], v[190:191], s[14:15], v[158:159] op_sel_hi:[1,0,1]
	v_readlane_b32 s14, v1, 32
	v_cvt_pk_f32_fp8_e32 v[184:185], v200
	v_cvt_pk_f32_fp8_sdwa v[186:187], v200 src0_sel:WORD_1
	v_pk_fma_f32 v[144:145], v[184:185], s[14:15], v[144:145] op_sel_hi:[1,0,1]
	v_pk_fma_f32 v[146:147], v[186:187], s[14:15], v[146:147] op_sel_hi:[1,0,1]
	v_cvt_pk_f32_fp8_e32 v[188:189], v201
	v_cvt_pk_f32_fp8_sdwa v[190:191], v201 src0_sel:WORD_1
	v_pk_fma_f32 v[148:149], v[188:189], s[14:15], v[148:149] op_sel_hi:[1,0,1]
	v_pk_fma_f32 v[150:151], v[190:191], s[14:15], v[150:151] op_sel_hi:[1,0,1]
	v_cvt_pk_f32_fp8_e32 v[184:185], v202
	v_cvt_pk_f32_fp8_sdwa v[186:187], v202 src0_sel:WORD_1
	v_pk_fma_f32 v[152:153], v[184:185], s[14:15], v[152:153] op_sel_hi:[1,0,1]
	v_pk_fma_f32 v[154:155], v[186:187], s[14:15], v[154:155] op_sel_hi:[1,0,1]
	v_cvt_pk_f32_fp8_e32 v[188:189], v203
	v_cvt_pk_f32_fp8_sdwa v[190:191], v203 src0_sel:WORD_1
	v_pk_fma_f32 v[156:157], v[188:189], s[14:15], v[156:157] op_sel_hi:[1,0,1]
	v_pk_fma_f32 v[158:159], v[190:191], s[14:15], v[158:159] op_sel_hi:[1,0,1]
	v_readlane_b32 s14, v1, 40
	v_cvt_pk_f32_fp8_e32 v[184:185], v204
	v_cvt_pk_f32_fp8_sdwa v[186:187], v204 src0_sel:WORD_1
	v_pk_fma_f32 v[144:145], v[184:185], s[14:15], v[144:145] op_sel_hi:[1,0,1]
	v_pk_fma_f32 v[146:147], v[186:187], s[14:15], v[146:147] op_sel_hi:[1,0,1]
	v_cvt_pk_f32_fp8_e32 v[188:189], v205
	v_cvt_pk_f32_fp8_sdwa v[190:191], v205 src0_sel:WORD_1
	v_pk_fma_f32 v[148:149], v[188:189], s[14:15], v[148:149] op_sel_hi:[1,0,1]
	v_pk_fma_f32 v[150:151], v[190:191], s[14:15], v[150:151] op_sel_hi:[1,0,1]
	v_cvt_pk_f32_fp8_e32 v[184:185], v206
	v_cvt_pk_f32_fp8_sdwa v[186:187], v206 src0_sel:WORD_1
	v_pk_fma_f32 v[152:153], v[184:185], s[14:15], v[152:153] op_sel_hi:[1,0,1]
	v_pk_fma_f32 v[154:155], v[186:187], s[14:15], v[154:155] op_sel_hi:[1,0,1]
	v_cvt_pk_f32_fp8_e32 v[188:189], v207
	v_cvt_pk_f32_fp8_sdwa v[190:191], v207 src0_sel:WORD_1
	v_pk_fma_f32 v[156:157], v[188:189], s[14:15], v[156:157] op_sel_hi:[1,0,1]
	v_pk_fma_f32 v[158:159], v[190:191], s[14:15], v[158:159] op_sel_hi:[1,0,1]
	v_readlane_b32 s14, v1, 48
	v_cvt_pk_f32_fp8_e32 v[184:185], v212
	v_cvt_pk_f32_fp8_sdwa v[186:187], v212 src0_sel:WORD_1
	v_pk_fma_f32 v[144:145], v[184:185], s[14:15], v[144:145] op_sel_hi:[1,0,1]
	v_pk_fma_f32 v[146:147], v[186:187], s[14:15], v[146:147] op_sel_hi:[1,0,1]
	v_cvt_pk_f32_fp8_e32 v[188:189], v213
	v_cvt_pk_f32_fp8_sdwa v[190:191], v213 src0_sel:WORD_1
	v_pk_fma_f32 v[148:149], v[188:189], s[14:15], v[148:149] op_sel_hi:[1,0,1]
	v_pk_fma_f32 v[150:151], v[190:191], s[14:15], v[150:151] op_sel_hi:[1,0,1]
	v_cvt_pk_f32_fp8_e32 v[184:185], v214
	v_cvt_pk_f32_fp8_sdwa v[186:187], v214 src0_sel:WORD_1
	v_pk_fma_f32 v[152:153], v[184:185], s[14:15], v[152:153] op_sel_hi:[1,0,1]
	v_pk_fma_f32 v[154:155], v[186:187], s[14:15], v[154:155] op_sel_hi:[1,0,1]
	v_cvt_pk_f32_fp8_e32 v[188:189], v215
	v_cvt_pk_f32_fp8_sdwa v[190:191], v215 src0_sel:WORD_1
	v_pk_fma_f32 v[156:157], v[188:189], s[14:15], v[156:157] op_sel_hi:[1,0,1]
	v_pk_fma_f32 v[158:159], v[190:191], s[14:15], v[158:159] op_sel_hi:[1,0,1]
	v_readlane_b32 s14, v1, 56
	v_cvt_pk_f32_fp8_e32 v[184:185], v220
	v_cvt_pk_f32_fp8_sdwa v[186:187], v220 src0_sel:WORD_1
	v_pk_fma_f32 v[144:145], v[184:185], s[14:15], v[144:145] op_sel_hi:[1,0,1]
	v_pk_fma_f32 v[146:147], v[186:187], s[14:15], v[146:147] op_sel_hi:[1,0,1]
	v_cvt_pk_f32_fp8_e32 v[188:189], v221
	v_cvt_pk_f32_fp8_sdwa v[190:191], v221 src0_sel:WORD_1
	v_pk_fma_f32 v[148:149], v[188:189], s[14:15], v[148:149] op_sel_hi:[1,0,1]
	v_pk_fma_f32 v[150:151], v[190:191], s[14:15], v[150:151] op_sel_hi:[1,0,1]
	v_cvt_pk_f32_fp8_e32 v[184:185], v222
	v_cvt_pk_f32_fp8_sdwa v[186:187], v222 src0_sel:WORD_1
	v_pk_fma_f32 v[152:153], v[184:185], s[14:15], v[152:153] op_sel_hi:[1,0,1]
	v_pk_fma_f32 v[154:155], v[186:187], s[14:15], v[154:155] op_sel_hi:[1,0,1]
	v_cvt_pk_f32_fp8_e32 v[188:189], v223
	v_cvt_pk_f32_fp8_sdwa v[190:191], v223 src0_sel:WORD_1
	v_pk_fma_f32 v[156:157], v[188:189], s[14:15], v[156:157] op_sel_hi:[1,0,1]
	v_pk_fma_f32 v[158:159], v[190:191], s[14:15], v[158:159] op_sel_hi:[1,0,1]
	s_branch .Lp6c2_axdone
.Lp6c2_t5:
	v_readlane_b32 s14, v1, 0
	v_cvt_pk_f32_fp8_e32 v[184:185], v4
	v_cvt_pk_f32_fp8_sdwa v[186:187], v4 src0_sel:WORD_1
	v_pk_fma_f32 v[160:161], v[184:185], s[14:15], v[160:161] op_sel_hi:[1,0,1]
	v_pk_fma_f32 v[162:163], v[186:187], s[14:15], v[162:163] op_sel_hi:[1,0,1]
	v_cvt_pk_f32_fp8_e32 v[188:189], v5
	v_cvt_pk_f32_fp8_sdwa v[190:191], v5 src0_sel:WORD_1
	v_pk_fma_f32 v[164:165], v[188:189], s[14:15], v[164:165] op_sel_hi:[1,0,1]
	v_pk_fma_f32 v[166:167], v[190:191], s[14:15], v[166:167] op_sel_hi:[1,0,1]
	v_cvt_pk_f32_fp8_e32 v[184:185], v6
	v_cvt_pk_f32_fp8_sdwa v[186:187], v6 src0_sel:WORD_1
	v_pk_fma_f32 v[168:169], v[184:185], s[14:15], v[168:169] op_sel_hi:[1,0,1]
	v_pk_fma_f32 v[170:171], v[186:187], s[14:15], v[170:171] op_sel_hi:[1,0,1]
	v_cvt_pk_f32_fp8_e32 v[188:189], v7
	v_cvt_pk_f32_fp8_sdwa v[190:191], v7 src0_sel:WORD_1
	v_pk_fma_f32 v[172:173], v[188:189], s[14:15], v[172:173] op_sel_hi:[1,0,1]
	v_pk_fma_f32 v[174:175], v[190:191], s[14:15], v[174:175] op_sel_hi:[1,0,1]
	v_readlane_b32 s14, v1, 8
	v_cvt_pk_f32_fp8_e32 v[184:185], v8
	v_cvt_pk_f32_fp8_sdwa v[186:187], v8 src0_sel:WORD_1
	v_pk_fma_f32 v[160:161], v[184:185], s[14:15], v[160:161] op_sel_hi:[1,0,1]
	v_pk_fma_f32 v[162:163], v[186:187], s[14:15], v[162:163] op_sel_hi:[1,0,1]
	v_cvt_pk_f32_fp8_e32 v[188:189], v9
	v_cvt_pk_f32_fp8_sdwa v[190:191], v9 src0_sel:WORD_1
	v_pk_fma_f32 v[164:165], v[188:189], s[14:15], v[164:165] op_sel_hi:[1,0,1]
	v_pk_fma_f32 v[166:167], v[190:191], s[14:15], v[166:167] op_sel_hi:[1,0,1]
	v_cvt_pk_f32_fp8_e32 v[184:185], v10
	v_cvt_pk_f32_fp8_sdwa v[186:187], v10 src0_sel:WORD_1
	v_pk_fma_f32 v[168:169], v[184:185], s[14:15], v[168:169] op_sel_hi:[1,0,1]
	v_pk_fma_f32 v[170:171], v[186:187], s[14:15], v[170:171] op_sel_hi:[1,0,1]
	v_cvt_pk_f32_fp8_e32 v[188:189], v11
	v_cvt_pk_f32_fp8_sdwa v[190:191], v11 src0_sel:WORD_1
	v_pk_fma_f32 v[172:173], v[188:189], s[14:15], v[172:173] op_sel_hi:[1,0,1]
	v_pk_fma_f32 v[174:175], v[190:191], s[14:15], v[174:175] op_sel_hi:[1,0,1]
	v_readlane_b32 s14, v1, 16
	v_cvt_pk_f32_fp8_e32 v[184:185], v192
	v_cvt_pk_f32_fp8_sdwa v[186:187], v192 src0_sel:WORD_1
	v_pk_fma_f32 v[160:161], v[184:185], s[14:15], v[160:161] op_sel_hi:[1,0,1]
	v_pk_fma_f32 v[162:163], v[186:187], s[14:15], v[162:163] op_sel_hi:[1,0,1]
	v_cvt_pk_f32_fp8_e32 v[188:189], v193
	v_cvt_pk_f32_fp8_sdwa v[190:191], v193 src0_sel:WORD_1
	v_pk_fma_f32 v[164:165], v[188:189], s[14:15], v[164:165] op_sel_hi:[1,0,1]
	v_pk_fma_f32 v[166:167], v[190:191], s[14:15], v[166:167] op_sel_hi:[1,0,1]
	v_cvt_pk_f32_fp8_e32 v[184:185], v194
	v_cvt_pk_f32_fp8_sdwa v[186:187], v194 src0_sel:WORD_1
	v_pk_fma_f32 v[168:169], v[184:185], s[14:15], v[168:169] op_sel_hi:[1,0,1]
	v_pk_fma_f32 v[170:171], v[186:187], s[14:15], v[170:171] op_sel_hi:[1,0,1]
	v_cvt_pk_f32_fp8_e32 v[188:189], v195
	v_cvt_pk_f32_fp8_sdwa v[190:191], v195 src0_sel:WORD_1
	v_pk_fma_f32 v[172:173], v[188:189], s[14:15], v[172:173] op_sel_hi:[1,0,1]
	v_pk_fma_f32 v[174:175], v[190:191], s[14:15], v[174:175] op_sel_hi:[1,0,1]
	v_readlane_b32 s14, v1, 24
	v_cvt_pk_f32_fp8_e32 v[184:185], v196
	v_cvt_pk_f32_fp8_sdwa v[186:187], v196 src0_sel:WORD_1
	v_pk_fma_f32 v[160:161], v[184:185], s[14:15], v[160:161] op_sel_hi:[1,0,1]
	v_pk_fma_f32 v[162:163], v[186:187], s[14:15], v[162:163] op_sel_hi:[1,0,1]
	v_cvt_pk_f32_fp8_e32 v[188:189], v197
	v_cvt_pk_f32_fp8_sdwa v[190:191], v197 src0_sel:WORD_1
	v_pk_fma_f32 v[164:165], v[188:189], s[14:15], v[164:165] op_sel_hi:[1,0,1]
	v_pk_fma_f32 v[166:167], v[190:191], s[14:15], v[166:167] op_sel_hi:[1,0,1]
	v_cvt_pk_f32_fp8_e32 v[184:185], v198
	v_cvt_pk_f32_fp8_sdwa v[186:187], v198 src0_sel:WORD_1
	v_pk_fma_f32 v[168:169], v[184:185], s[14:15], v[168:169] op_sel_hi:[1,0,1]
	v_pk_fma_f32 v[170:171], v[186:187], s[14:15], v[170:171] op_sel_hi:[1,0,1]
	v_cvt_pk_f32_fp8_e32 v[188:189], v199
	v_cvt_pk_f32_fp8_sdwa v[190:191], v199 src0_sel:WORD_1
	v_pk_fma_f32 v[172:173], v[188:189], s[14:15], v[172:173] op_sel_hi:[1,0,1]
	v_pk_fma_f32 v[174:175], v[190:191], s[14:15], v[174:175] op_sel_hi:[1,0,1]
	v_readlane_b32 s14, v1, 32
	v_cvt_pk_f32_fp8_e32 v[184:185], v200
	v_cvt_pk_f32_fp8_sdwa v[186:187], v200 src0_sel:WORD_1
	v_pk_fma_f32 v[160:161], v[184:185], s[14:15], v[160:161] op_sel_hi:[1,0,1]
	v_pk_fma_f32 v[162:163], v[186:187], s[14:15], v[162:163] op_sel_hi:[1,0,1]
	v_cvt_pk_f32_fp8_e32 v[188:189], v201
	v_cvt_pk_f32_fp8_sdwa v[190:191], v201 src0_sel:WORD_1
	v_pk_fma_f32 v[164:165], v[188:189], s[14:15], v[164:165] op_sel_hi:[1,0,1]
	v_pk_fma_f32 v[166:167], v[190:191], s[14:15], v[166:167] op_sel_hi:[1,0,1]
	v_cvt_pk_f32_fp8_e32 v[184:185], v202
	v_cvt_pk_f32_fp8_sdwa v[186:187], v202 src0_sel:WORD_1
	v_pk_fma_f32 v[168:169], v[184:185], s[14:15], v[168:169] op_sel_hi:[1,0,1]
	v_pk_fma_f32 v[170:171], v[186:187], s[14:15], v[170:171] op_sel_hi:[1,0,1]
	v_cvt_pk_f32_fp8_e32 v[188:189], v203
	v_cvt_pk_f32_fp8_sdwa v[190:191], v203 src0_sel:WORD_1
	v_pk_fma_f32 v[172:173], v[188:189], s[14:15], v[172:173] op_sel_hi:[1,0,1]
	v_pk_fma_f32 v[174:175], v[190:191], s[14:15], v[174:175] op_sel_hi:[1,0,1]
	v_readlane_b32 s14, v1, 40
	v_cvt_pk_f32_fp8_e32 v[184:185], v204
	v_cvt_pk_f32_fp8_sdwa v[186:187], v204 src0_sel:WORD_1
	v_pk_fma_f32 v[160:161], v[184:185], s[14:15], v[160:161] op_sel_hi:[1,0,1]
	v_pk_fma_f32 v[162:163], v[186:187], s[14:15], v[162:163] op_sel_hi:[1,0,1]
	v_cvt_pk_f32_fp8_e32 v[188:189], v205
	v_cvt_pk_f32_fp8_sdwa v[190:191], v205 src0_sel:WORD_1
	v_pk_fma_f32 v[164:165], v[188:189], s[14:15], v[164:165] op_sel_hi:[1,0,1]
	v_pk_fma_f32 v[166:167], v[190:191], s[14:15], v[166:167] op_sel_hi:[1,0,1]
	v_cvt_pk_f32_fp8_e32 v[184:185], v206
	v_cvt_pk_f32_fp8_sdwa v[186:187], v206 src0_sel:WORD_1
	v_pk_fma_f32 v[168:169], v[184:185], s[14:15], v[168:169] op_sel_hi:[1,0,1]
	v_pk_fma_f32 v[170:171], v[186:187], s[14:15], v[170:171] op_sel_hi:[1,0,1]
	v_cvt_pk_f32_fp8_e32 v[188:189], v207
	v_cvt_pk_f32_fp8_sdwa v[190:191], v207 src0_sel:WORD_1
	v_pk_fma_f32 v[172:173], v[188:189], s[14:15], v[172:173] op_sel_hi:[1,0,1]
	v_pk_fma_f32 v[174:175], v[190:191], s[14:15], v[174:175] op_sel_hi:[1,0,1]
	v_readlane_b32 s14, v1, 48
	v_cvt_pk_f32_fp8_e32 v[184:185], v212
	v_cvt_pk_f32_fp8_sdwa v[186:187], v212 src0_sel:WORD_1
	v_pk_fma_f32 v[160:161], v[184:185], s[14:15], v[160:161] op_sel_hi:[1,0,1]
	v_pk_fma_f32 v[162:163], v[186:187], s[14:15], v[162:163] op_sel_hi:[1,0,1]
	v_cvt_pk_f32_fp8_e32 v[188:189], v213
	v_cvt_pk_f32_fp8_sdwa v[190:191], v213 src0_sel:WORD_1
	v_pk_fma_f32 v[164:165], v[188:189], s[14:15], v[164:165] op_sel_hi:[1,0,1]
	v_pk_fma_f32 v[166:167], v[190:191], s[14:15], v[166:167] op_sel_hi:[1,0,1]
	v_cvt_pk_f32_fp8_e32 v[184:185], v214
	v_cvt_pk_f32_fp8_sdwa v[186:187], v214 src0_sel:WORD_1
	v_pk_fma_f32 v[168:169], v[184:185], s[14:15], v[168:169] op_sel_hi:[1,0,1]
	v_pk_fma_f32 v[170:171], v[186:187], s[14:15], v[170:171] op_sel_hi:[1,0,1]
	v_cvt_pk_f32_fp8_e32 v[188:189], v215
	v_cvt_pk_f32_fp8_sdwa v[190:191], v215 src0_sel:WORD_1
	v_pk_fma_f32 v[172:173], v[188:189], s[14:15], v[172:173] op_sel_hi:[1,0,1]
	v_pk_fma_f32 v[174:175], v[190:191], s[14:15], v[174:175] op_sel_hi:[1,0,1]
	v_readlane_b32 s14, v1, 56
	v_cvt_pk_f32_fp8_e32 v[184:185], v220
	v_cvt_pk_f32_fp8_sdwa v[186:187], v220 src0_sel:WORD_1
	v_pk_fma_f32 v[160:161], v[184:185], s[14:15], v[160:161] op_sel_hi:[1,0,1]
	v_pk_fma_f32 v[162:163], v[186:187], s[14:15], v[162:163] op_sel_hi:[1,0,1]
	v_cvt_pk_f32_fp8_e32 v[188:189], v221
	v_cvt_pk_f32_fp8_sdwa v[190:191], v221 src0_sel:WORD_1
	v_pk_fma_f32 v[164:165], v[188:189], s[14:15], v[164:165] op_sel_hi:[1,0,1]
	v_pk_fma_f32 v[166:167], v[190:191], s[14:15], v[166:167] op_sel_hi:[1,0,1]
	v_cvt_pk_f32_fp8_e32 v[184:185], v222
	v_cvt_pk_f32_fp8_sdwa v[186:187], v222 src0_sel:WORD_1
	v_pk_fma_f32 v[168:169], v[184:185], s[14:15], v[168:169] op_sel_hi:[1,0,1]
	v_pk_fma_f32 v[170:171], v[186:187], s[14:15], v[170:171] op_sel_hi:[1,0,1]
	v_cvt_pk_f32_fp8_e32 v[188:189], v223
	v_cvt_pk_f32_fp8_sdwa v[190:191], v223 src0_sel:WORD_1
	v_pk_fma_f32 v[172:173], v[188:189], s[14:15], v[172:173] op_sel_hi:[1,0,1]
	v_pk_fma_f32 v[174:175], v[190:191], s[14:15], v[174:175] op_sel_hi:[1,0,1]
	s_branch .Lp6c2_axdone
.Lp6c2_t6:
	v_readlane_b32 s14, v1, 0
	v_cvt_pk_f32_fp8_e32 v[184:185], v4
	v_cvt_pk_f32_fp8_sdwa v[186:187], v4 src0_sel:WORD_1
	v_pk_fma_f32 v[224:225], v[184:185], s[14:15], v[224:225] op_sel_hi:[1,0,1]
	v_pk_fma_f32 v[226:227], v[186:187], s[14:15], v[226:227] op_sel_hi:[1,0,1]
	v_cvt_pk_f32_fp8_e32 v[188:189], v5
	v_cvt_pk_f32_fp8_sdwa v[190:191], v5 src0_sel:WORD_1
	v_pk_fma_f32 v[228:229], v[188:189], s[14:15], v[228:229] op_sel_hi:[1,0,1]
	v_pk_fma_f32 v[230:231], v[190:191], s[14:15], v[230:231] op_sel_hi:[1,0,1]
	v_cvt_pk_f32_fp8_e32 v[184:185], v6
	v_cvt_pk_f32_fp8_sdwa v[186:187], v6 src0_sel:WORD_1
	v_pk_fma_f32 v[232:233], v[184:185], s[14:15], v[232:233] op_sel_hi:[1,0,1]
	v_pk_fma_f32 v[234:235], v[186:187], s[14:15], v[234:235] op_sel_hi:[1,0,1]
	v_cvt_pk_f32_fp8_e32 v[188:189], v7
	v_cvt_pk_f32_fp8_sdwa v[190:191], v7 src0_sel:WORD_1
	v_pk_fma_f32 v[236:237], v[188:189], s[14:15], v[236:237] op_sel_hi:[1,0,1]
	v_pk_fma_f32 v[238:239], v[190:191], s[14:15], v[238:239] op_sel_hi:[1,0,1]
	v_readlane_b32 s14, v1, 8
	v_cvt_pk_f32_fp8_e32 v[184:185], v8
	v_cvt_pk_f32_fp8_sdwa v[186:187], v8 src0_sel:WORD_1
	v_pk_fma_f32 v[224:225], v[184:185], s[14:15], v[224:225] op_sel_hi:[1,0,1]
	v_pk_fma_f32 v[226:227], v[186:187], s[14:15], v[226:227] op_sel_hi:[1,0,1]
	v_cvt_pk_f32_fp8_e32 v[188:189], v9
	v_cvt_pk_f32_fp8_sdwa v[190:191], v9 src0_sel:WORD_1
	v_pk_fma_f32 v[228:229], v[188:189], s[14:15], v[228:229] op_sel_hi:[1,0,1]
	v_pk_fma_f32 v[230:231], v[190:191], s[14:15], v[230:231] op_sel_hi:[1,0,1]
	v_cvt_pk_f32_fp8_e32 v[184:185], v10
	v_cvt_pk_f32_fp8_sdwa v[186:187], v10 src0_sel:WORD_1
	v_pk_fma_f32 v[232:233], v[184:185], s[14:15], v[232:233] op_sel_hi:[1,0,1]
	v_pk_fma_f32 v[234:235], v[186:187], s[14:15], v[234:235] op_sel_hi:[1,0,1]
	v_cvt_pk_f32_fp8_e32 v[188:189], v11
	v_cvt_pk_f32_fp8_sdwa v[190:191], v11 src0_sel:WORD_1
	v_pk_fma_f32 v[236:237], v[188:189], s[14:15], v[236:237] op_sel_hi:[1,0,1]
	v_pk_fma_f32 v[238:239], v[190:191], s[14:15], v[238:239] op_sel_hi:[1,0,1]
	v_readlane_b32 s14, v1, 16
	v_cvt_pk_f32_fp8_e32 v[184:185], v192
	v_cvt_pk_f32_fp8_sdwa v[186:187], v192 src0_sel:WORD_1
	v_pk_fma_f32 v[224:225], v[184:185], s[14:15], v[224:225] op_sel_hi:[1,0,1]
	v_pk_fma_f32 v[226:227], v[186:187], s[14:15], v[226:227] op_sel_hi:[1,0,1]
	v_cvt_pk_f32_fp8_e32 v[188:189], v193
	v_cvt_pk_f32_fp8_sdwa v[190:191], v193 src0_sel:WORD_1
	v_pk_fma_f32 v[228:229], v[188:189], s[14:15], v[228:229] op_sel_hi:[1,0,1]
	v_pk_fma_f32 v[230:231], v[190:191], s[14:15], v[230:231] op_sel_hi:[1,0,1]
	v_cvt_pk_f32_fp8_e32 v[184:185], v194
	v_cvt_pk_f32_fp8_sdwa v[186:187], v194 src0_sel:WORD_1
	v_pk_fma_f32 v[232:233], v[184:185], s[14:15], v[232:233] op_sel_hi:[1,0,1]
	v_pk_fma_f32 v[234:235], v[186:187], s[14:15], v[234:235] op_sel_hi:[1,0,1]
	v_cvt_pk_f32_fp8_e32 v[188:189], v195
	v_cvt_pk_f32_fp8_sdwa v[190:191], v195 src0_sel:WORD_1
	v_pk_fma_f32 v[236:237], v[188:189], s[14:15], v[236:237] op_sel_hi:[1,0,1]
	v_pk_fma_f32 v[238:239], v[190:191], s[14:15], v[238:239] op_sel_hi:[1,0,1]
	v_readlane_b32 s14, v1, 24
	v_cvt_pk_f32_fp8_e32 v[184:185], v196
	v_cvt_pk_f32_fp8_sdwa v[186:187], v196 src0_sel:WORD_1
	v_pk_fma_f32 v[224:225], v[184:185], s[14:15], v[224:225] op_sel_hi:[1,0,1]
	v_pk_fma_f32 v[226:227], v[186:187], s[14:15], v[226:227] op_sel_hi:[1,0,1]
	v_cvt_pk_f32_fp8_e32 v[188:189], v197
	v_cvt_pk_f32_fp8_sdwa v[190:191], v197 src0_sel:WORD_1
	v_pk_fma_f32 v[228:229], v[188:189], s[14:15], v[228:229] op_sel_hi:[1,0,1]
	v_pk_fma_f32 v[230:231], v[190:191], s[14:15], v[230:231] op_sel_hi:[1,0,1]
	v_cvt_pk_f32_fp8_e32 v[184:185], v198
	v_cvt_pk_f32_fp8_sdwa v[186:187], v198 src0_sel:WORD_1
	v_pk_fma_f32 v[232:233], v[184:185], s[14:15], v[232:233] op_sel_hi:[1,0,1]
	v_pk_fma_f32 v[234:235], v[186:187], s[14:15], v[234:235] op_sel_hi:[1,0,1]
	v_cvt_pk_f32_fp8_e32 v[188:189], v199
	v_cvt_pk_f32_fp8_sdwa v[190:191], v199 src0_sel:WORD_1
	v_pk_fma_f32 v[236:237], v[188:189], s[14:15], v[236:237] op_sel_hi:[1,0,1]
	v_pk_fma_f32 v[238:239], v[190:191], s[14:15], v[238:239] op_sel_hi:[1,0,1]
	v_readlane_b32 s14, v1, 32
	v_cvt_pk_f32_fp8_e32 v[184:185], v200
	v_cvt_pk_f32_fp8_sdwa v[186:187], v200 src0_sel:WORD_1
	v_pk_fma_f32 v[224:225], v[184:185], s[14:15], v[224:225] op_sel_hi:[1,0,1]
	v_pk_fma_f32 v[226:227], v[186:187], s[14:15], v[226:227] op_sel_hi:[1,0,1]
	v_cvt_pk_f32_fp8_e32 v[188:189], v201
	v_cvt_pk_f32_fp8_sdwa v[190:191], v201 src0_sel:WORD_1
	v_pk_fma_f32 v[228:229], v[188:189], s[14:15], v[228:229] op_sel_hi:[1,0,1]
	v_pk_fma_f32 v[230:231], v[190:191], s[14:15], v[230:231] op_sel_hi:[1,0,1]
	v_cvt_pk_f32_fp8_e32 v[184:185], v202
	v_cvt_pk_f32_fp8_sdwa v[186:187], v202 src0_sel:WORD_1
	v_pk_fma_f32 v[232:233], v[184:185], s[14:15], v[232:233] op_sel_hi:[1,0,1]
	v_pk_fma_f32 v[234:235], v[186:187], s[14:15], v[234:235] op_sel_hi:[1,0,1]
	v_cvt_pk_f32_fp8_e32 v[188:189], v203
	v_cvt_pk_f32_fp8_sdwa v[190:191], v203 src0_sel:WORD_1
	v_pk_fma_f32 v[236:237], v[188:189], s[14:15], v[236:237] op_sel_hi:[1,0,1]
	v_pk_fma_f32 v[238:239], v[190:191], s[14:15], v[238:239] op_sel_hi:[1,0,1]
	v_readlane_b32 s14, v1, 40
	v_cvt_pk_f32_fp8_e32 v[184:185], v204
	v_cvt_pk_f32_fp8_sdwa v[186:187], v204 src0_sel:WORD_1
	v_pk_fma_f32 v[224:225], v[184:185], s[14:15], v[224:225] op_sel_hi:[1,0,1]
	v_pk_fma_f32 v[226:227], v[186:187], s[14:15], v[226:227] op_sel_hi:[1,0,1]
	v_cvt_pk_f32_fp8_e32 v[188:189], v205
	v_cvt_pk_f32_fp8_sdwa v[190:191], v205 src0_sel:WORD_1
	v_pk_fma_f32 v[228:229], v[188:189], s[14:15], v[228:229] op_sel_hi:[1,0,1]
	v_pk_fma_f32 v[230:231], v[190:191], s[14:15], v[230:231] op_sel_hi:[1,0,1]
	v_cvt_pk_f32_fp8_e32 v[184:185], v206
	v_cvt_pk_f32_fp8_sdwa v[186:187], v206 src0_sel:WORD_1
	v_pk_fma_f32 v[232:233], v[184:185], s[14:15], v[232:233] op_sel_hi:[1,0,1]
	v_pk_fma_f32 v[234:235], v[186:187], s[14:15], v[234:235] op_sel_hi:[1,0,1]
	v_cvt_pk_f32_fp8_e32 v[188:189], v207
	v_cvt_pk_f32_fp8_sdwa v[190:191], v207 src0_sel:WORD_1
	v_pk_fma_f32 v[236:237], v[188:189], s[14:15], v[236:237] op_sel_hi:[1,0,1]
	v_pk_fma_f32 v[238:239], v[190:191], s[14:15], v[238:239] op_sel_hi:[1,0,1]
	v_readlane_b32 s14, v1, 48
	v_cvt_pk_f32_fp8_e32 v[184:185], v212
	v_cvt_pk_f32_fp8_sdwa v[186:187], v212 src0_sel:WORD_1
	v_pk_fma_f32 v[224:225], v[184:185], s[14:15], v[224:225] op_sel_hi:[1,0,1]
	v_pk_fma_f32 v[226:227], v[186:187], s[14:15], v[226:227] op_sel_hi:[1,0,1]
	v_cvt_pk_f32_fp8_e32 v[188:189], v213
	v_cvt_pk_f32_fp8_sdwa v[190:191], v213 src0_sel:WORD_1
	v_pk_fma_f32 v[228:229], v[188:189], s[14:15], v[228:229] op_sel_hi:[1,0,1]
	v_pk_fma_f32 v[230:231], v[190:191], s[14:15], v[230:231] op_sel_hi:[1,0,1]
	v_cvt_pk_f32_fp8_e32 v[184:185], v214
	v_cvt_pk_f32_fp8_sdwa v[186:187], v214 src0_sel:WORD_1
	v_pk_fma_f32 v[232:233], v[184:185], s[14:15], v[232:233] op_sel_hi:[1,0,1]
	v_pk_fma_f32 v[234:235], v[186:187], s[14:15], v[234:235] op_sel_hi:[1,0,1]
	v_cvt_pk_f32_fp8_e32 v[188:189], v215
	v_cvt_pk_f32_fp8_sdwa v[190:191], v215 src0_sel:WORD_1
	v_pk_fma_f32 v[236:237], v[188:189], s[14:15], v[236:237] op_sel_hi:[1,0,1]
	v_pk_fma_f32 v[238:239], v[190:191], s[14:15], v[238:239] op_sel_hi:[1,0,1]
	v_readlane_b32 s14, v1, 56
	v_cvt_pk_f32_fp8_e32 v[184:185], v220
	v_cvt_pk_f32_fp8_sdwa v[186:187], v220 src0_sel:WORD_1
	v_pk_fma_f32 v[224:225], v[184:185], s[14:15], v[224:225] op_sel_hi:[1,0,1]
	v_pk_fma_f32 v[226:227], v[186:187], s[14:15], v[226:227] op_sel_hi:[1,0,1]
	v_cvt_pk_f32_fp8_e32 v[188:189], v221
	v_cvt_pk_f32_fp8_sdwa v[190:191], v221 src0_sel:WORD_1
	v_pk_fma_f32 v[228:229], v[188:189], s[14:15], v[228:229] op_sel_hi:[1,0,1]
	v_pk_fma_f32 v[230:231], v[190:191], s[14:15], v[230:231] op_sel_hi:[1,0,1]
	v_cvt_pk_f32_fp8_e32 v[184:185], v222
	v_cvt_pk_f32_fp8_sdwa v[186:187], v222 src0_sel:WORD_1
	v_pk_fma_f32 v[232:233], v[184:185], s[14:15], v[232:233] op_sel_hi:[1,0,1]
	v_pk_fma_f32 v[234:235], v[186:187], s[14:15], v[234:235] op_sel_hi:[1,0,1]
	v_cvt_pk_f32_fp8_e32 v[188:189], v223
	v_cvt_pk_f32_fp8_sdwa v[190:191], v223 src0_sel:WORD_1
	v_pk_fma_f32 v[236:237], v[188:189], s[14:15], v[236:237] op_sel_hi:[1,0,1]
	v_pk_fma_f32 v[238:239], v[190:191], s[14:15], v[238:239] op_sel_hi:[1,0,1]
	s_branch .Lp6c2_axdone
.Lp6c2_t7:
	v_readlane_b32 s14, v1, 0
	v_cvt_pk_f32_fp8_e32 v[184:185], v4
	v_cvt_pk_f32_fp8_sdwa v[186:187], v4 src0_sel:WORD_1
	v_pk_fma_f32 v[240:241], v[184:185], s[14:15], v[240:241] op_sel_hi:[1,0,1]
	v_pk_fma_f32 v[242:243], v[186:187], s[14:15], v[242:243] op_sel_hi:[1,0,1]
	v_cvt_pk_f32_fp8_e32 v[188:189], v5
	v_cvt_pk_f32_fp8_sdwa v[190:191], v5 src0_sel:WORD_1
	v_pk_fma_f32 v[244:245], v[188:189], s[14:15], v[244:245] op_sel_hi:[1,0,1]
	v_pk_fma_f32 v[246:247], v[190:191], s[14:15], v[246:247] op_sel_hi:[1,0,1]
	v_cvt_pk_f32_fp8_e32 v[184:185], v6
	v_cvt_pk_f32_fp8_sdwa v[186:187], v6 src0_sel:WORD_1
	v_pk_fma_f32 v[248:249], v[184:185], s[14:15], v[248:249] op_sel_hi:[1,0,1]
	v_pk_fma_f32 v[250:251], v[186:187], s[14:15], v[250:251] op_sel_hi:[1,0,1]
	v_cvt_pk_f32_fp8_e32 v[188:189], v7
	v_cvt_pk_f32_fp8_sdwa v[190:191], v7 src0_sel:WORD_1
	v_pk_fma_f32 v[216:217], v[188:189], s[14:15], v[216:217] op_sel_hi:[1,0,1]
	v_pk_fma_f32 v[218:219], v[190:191], s[14:15], v[218:219] op_sel_hi:[1,0,1]
	v_readlane_b32 s14, v1, 8
	v_cvt_pk_f32_fp8_e32 v[184:185], v8
	v_cvt_pk_f32_fp8_sdwa v[186:187], v8 src0_sel:WORD_1
	v_pk_fma_f32 v[240:241], v[184:185], s[14:15], v[240:241] op_sel_hi:[1,0,1]
	v_pk_fma_f32 v[242:243], v[186:187], s[14:15], v[242:243] op_sel_hi:[1,0,1]
	v_cvt_pk_f32_fp8_e32 v[188:189], v9
	v_cvt_pk_f32_fp8_sdwa v[190:191], v9 src0_sel:WORD_1
	v_pk_fma_f32 v[244:245], v[188:189], s[14:15], v[244:245] op_sel_hi:[1,0,1]
	v_pk_fma_f32 v[246:247], v[190:191], s[14:15], v[246:247] op_sel_hi:[1,0,1]
	v_cvt_pk_f32_fp8_e32 v[184:185], v10
	v_cvt_pk_f32_fp8_sdwa v[186:187], v10 src0_sel:WORD_1
	v_pk_fma_f32 v[248:249], v[184:185], s[14:15], v[248:249] op_sel_hi:[1,0,1]
	v_pk_fma_f32 v[250:251], v[186:187], s[14:15], v[250:251] op_sel_hi:[1,0,1]
	v_cvt_pk_f32_fp8_e32 v[188:189], v11
	v_cvt_pk_f32_fp8_sdwa v[190:191], v11 src0_sel:WORD_1
	v_pk_fma_f32 v[216:217], v[188:189], s[14:15], v[216:217] op_sel_hi:[1,0,1]
	v_pk_fma_f32 v[218:219], v[190:191], s[14:15], v[218:219] op_sel_hi:[1,0,1]
	v_readlane_b32 s14, v1, 16
	v_cvt_pk_f32_fp8_e32 v[184:185], v192
	v_cvt_pk_f32_fp8_sdwa v[186:187], v192 src0_sel:WORD_1
	v_pk_fma_f32 v[240:241], v[184:185], s[14:15], v[240:241] op_sel_hi:[1,0,1]
	v_pk_fma_f32 v[242:243], v[186:187], s[14:15], v[242:243] op_sel_hi:[1,0,1]
	v_cvt_pk_f32_fp8_e32 v[188:189], v193
	v_cvt_pk_f32_fp8_sdwa v[190:191], v193 src0_sel:WORD_1
	v_pk_fma_f32 v[244:245], v[188:189], s[14:15], v[244:245] op_sel_hi:[1,0,1]
	v_pk_fma_f32 v[246:247], v[190:191], s[14:15], v[246:247] op_sel_hi:[1,0,1]
	v_cvt_pk_f32_fp8_e32 v[184:185], v194
	v_cvt_pk_f32_fp8_sdwa v[186:187], v194 src0_sel:WORD_1
	v_pk_fma_f32 v[248:249], v[184:185], s[14:15], v[248:249] op_sel_hi:[1,0,1]
	v_pk_fma_f32 v[250:251], v[186:187], s[14:15], v[250:251] op_sel_hi:[1,0,1]
	v_cvt_pk_f32_fp8_e32 v[188:189], v195
	v_cvt_pk_f32_fp8_sdwa v[190:191], v195 src0_sel:WORD_1
	v_pk_fma_f32 v[216:217], v[188:189], s[14:15], v[216:217] op_sel_hi:[1,0,1]
	v_pk_fma_f32 v[218:219], v[190:191], s[14:15], v[218:219] op_sel_hi:[1,0,1]
	v_readlane_b32 s14, v1, 24
	v_cvt_pk_f32_fp8_e32 v[184:185], v196
	v_cvt_pk_f32_fp8_sdwa v[186:187], v196 src0_sel:WORD_1
	v_pk_fma_f32 v[240:241], v[184:185], s[14:15], v[240:241] op_sel_hi:[1,0,1]
	v_pk_fma_f32 v[242:243], v[186:187], s[14:15], v[242:243] op_sel_hi:[1,0,1]
	v_cvt_pk_f32_fp8_e32 v[188:189], v197
	v_cvt_pk_f32_fp8_sdwa v[190:191], v197 src0_sel:WORD_1
	v_pk_fma_f32 v[244:245], v[188:189], s[14:15], v[244:245] op_sel_hi:[1,0,1]
	v_pk_fma_f32 v[246:247], v[190:191], s[14:15], v[246:247] op_sel_hi:[1,0,1]
	v_cvt_pk_f32_fp8_e32 v[184:185], v198
	v_cvt_pk_f32_fp8_sdwa v[186:187], v198 src0_sel:WORD_1
	v_pk_fma_f32 v[248:249], v[184:185], s[14:15], v[248:249] op_sel_hi:[1,0,1]
	v_pk_fma_f32 v[250:251], v[186:187], s[14:15], v[250:251] op_sel_hi:[1,0,1]
	v_cvt_pk_f32_fp8_e32 v[188:189], v199
	v_cvt_pk_f32_fp8_sdwa v[190:191], v199 src0_sel:WORD_1
	v_pk_fma_f32 v[216:217], v[188:189], s[14:15], v[216:217] op_sel_hi:[1,0,1]
	v_pk_fma_f32 v[218:219], v[190:191], s[14:15], v[218:219] op_sel_hi:[1,0,1]
	v_readlane_b32 s14, v1, 32
	v_cvt_pk_f32_fp8_e32 v[184:185], v200
	v_cvt_pk_f32_fp8_sdwa v[186:187], v200 src0_sel:WORD_1
	v_pk_fma_f32 v[240:241], v[184:185], s[14:15], v[240:241] op_sel_hi:[1,0,1]
	v_pk_fma_f32 v[242:243], v[186:187], s[14:15], v[242:243] op_sel_hi:[1,0,1]
	v_cvt_pk_f32_fp8_e32 v[188:189], v201
	v_cvt_pk_f32_fp8_sdwa v[190:191], v201 src0_sel:WORD_1
	v_pk_fma_f32 v[244:245], v[188:189], s[14:15], v[244:245] op_sel_hi:[1,0,1]
	v_pk_fma_f32 v[246:247], v[190:191], s[14:15], v[246:247] op_sel_hi:[1,0,1]
	v_cvt_pk_f32_fp8_e32 v[184:185], v202
	v_cvt_pk_f32_fp8_sdwa v[186:187], v202 src0_sel:WORD_1
	v_pk_fma_f32 v[248:249], v[184:185], s[14:15], v[248:249] op_sel_hi:[1,0,1]
	v_pk_fma_f32 v[250:251], v[186:187], s[14:15], v[250:251] op_sel_hi:[1,0,1]
	v_cvt_pk_f32_fp8_e32 v[188:189], v203
	v_cvt_pk_f32_fp8_sdwa v[190:191], v203 src0_sel:WORD_1
	v_pk_fma_f32 v[216:217], v[188:189], s[14:15], v[216:217] op_sel_hi:[1,0,1]
	v_pk_fma_f32 v[218:219], v[190:191], s[14:15], v[218:219] op_sel_hi:[1,0,1]
	v_readlane_b32 s14, v1, 40
	v_cvt_pk_f32_fp8_e32 v[184:185], v204
	v_cvt_pk_f32_fp8_sdwa v[186:187], v204 src0_sel:WORD_1
	v_pk_fma_f32 v[240:241], v[184:185], s[14:15], v[240:241] op_sel_hi:[1,0,1]
	v_pk_fma_f32 v[242:243], v[186:187], s[14:15], v[242:243] op_sel_hi:[1,0,1]
	v_cvt_pk_f32_fp8_e32 v[188:189], v205
	v_cvt_pk_f32_fp8_sdwa v[190:191], v205 src0_sel:WORD_1
	v_pk_fma_f32 v[244:245], v[188:189], s[14:15], v[244:245] op_sel_hi:[1,0,1]
	v_pk_fma_f32 v[246:247], v[190:191], s[14:15], v[246:247] op_sel_hi:[1,0,1]
	v_cvt_pk_f32_fp8_e32 v[184:185], v206
	v_cvt_pk_f32_fp8_sdwa v[186:187], v206 src0_sel:WORD_1
	v_pk_fma_f32 v[248:249], v[184:185], s[14:15], v[248:249] op_sel_hi:[1,0,1]
	v_pk_fma_f32 v[250:251], v[186:187], s[14:15], v[250:251] op_sel_hi:[1,0,1]
	v_cvt_pk_f32_fp8_e32 v[188:189], v207
	v_cvt_pk_f32_fp8_sdwa v[190:191], v207 src0_sel:WORD_1
	v_pk_fma_f32 v[216:217], v[188:189], s[14:15], v[216:217] op_sel_hi:[1,0,1]
	v_pk_fma_f32 v[218:219], v[190:191], s[14:15], v[218:219] op_sel_hi:[1,0,1]
	v_readlane_b32 s14, v1, 48
	v_cvt_pk_f32_fp8_e32 v[184:185], v212
	v_cvt_pk_f32_fp8_sdwa v[186:187], v212 src0_sel:WORD_1
	v_pk_fma_f32 v[240:241], v[184:185], s[14:15], v[240:241] op_sel_hi:[1,0,1]
	v_pk_fma_f32 v[242:243], v[186:187], s[14:15], v[242:243] op_sel_hi:[1,0,1]
	v_cvt_pk_f32_fp8_e32 v[188:189], v213
	v_cvt_pk_f32_fp8_sdwa v[190:191], v213 src0_sel:WORD_1
	v_pk_fma_f32 v[244:245], v[188:189], s[14:15], v[244:245] op_sel_hi:[1,0,1]
	v_pk_fma_f32 v[246:247], v[190:191], s[14:15], v[246:247] op_sel_hi:[1,0,1]
	v_cvt_pk_f32_fp8_e32 v[184:185], v214
	v_cvt_pk_f32_fp8_sdwa v[186:187], v214 src0_sel:WORD_1
	v_pk_fma_f32 v[248:249], v[184:185], s[14:15], v[248:249] op_sel_hi:[1,0,1]
	v_pk_fma_f32 v[250:251], v[186:187], s[14:15], v[250:251] op_sel_hi:[1,0,1]
	v_cvt_pk_f32_fp8_e32 v[188:189], v215
	v_cvt_pk_f32_fp8_sdwa v[190:191], v215 src0_sel:WORD_1
	v_pk_fma_f32 v[216:217], v[188:189], s[14:15], v[216:217] op_sel_hi:[1,0,1]
	v_pk_fma_f32 v[218:219], v[190:191], s[14:15], v[218:219] op_sel_hi:[1,0,1]
	v_readlane_b32 s14, v1, 56
	v_cvt_pk_f32_fp8_e32 v[184:185], v220
	v_cvt_pk_f32_fp8_sdwa v[186:187], v220 src0_sel:WORD_1
	v_pk_fma_f32 v[240:241], v[184:185], s[14:15], v[240:241] op_sel_hi:[1,0,1]
	v_pk_fma_f32 v[242:243], v[186:187], s[14:15], v[242:243] op_sel_hi:[1,0,1]
	v_cvt_pk_f32_fp8_e32 v[188:189], v221
	v_cvt_pk_f32_fp8_sdwa v[190:191], v221 src0_sel:WORD_1
	v_pk_fma_f32 v[244:245], v[188:189], s[14:15], v[244:245] op_sel_hi:[1,0,1]
	v_pk_fma_f32 v[246:247], v[190:191], s[14:15], v[246:247] op_sel_hi:[1,0,1]
	v_cvt_pk_f32_fp8_e32 v[184:185], v222
	v_cvt_pk_f32_fp8_sdwa v[186:187], v222 src0_sel:WORD_1
	v_pk_fma_f32 v[248:249], v[184:185], s[14:15], v[248:249] op_sel_hi:[1,0,1]
	v_pk_fma_f32 v[250:251], v[186:187], s[14:15], v[250:251] op_sel_hi:[1,0,1]
	v_cvt_pk_f32_fp8_e32 v[188:189], v223
	v_cvt_pk_f32_fp8_sdwa v[190:191], v223 src0_sel:WORD_1
	v_pk_fma_f32 v[216:217], v[188:189], s[14:15], v[216:217] op_sel_hi:[1,0,1]
	v_pk_fma_f32 v[218:219], v[190:191], s[14:15], v[218:219] op_sel_hi:[1,0,1]
	s_branch .Lp6c2_axdone
.Lp6c2_axdone:
	s_nop 4
	buffer_load_dwordx4 v[4:7], v181, s[92:95], s44 offen
	buffer_load_dwordx4 v[8:11], v181, s[92:95], s45 offen
	buffer_load_dwordx4 v[192:195], v181, s[92:95], s46 offen
	buffer_load_dwordx4 v[196:199], v181, s[92:95], s47 offen
	buffer_load_dwordx4 v[200:203], v181, s[92:95], s48 offen
	buffer_load_dwordx4 v[204:207], v181, s[92:95], s49 offen
	buffer_load_dwordx4 v[212:215], v181, s[92:95], s50 offen
	buffer_load_dwordx4 v[220:223], v181, s[92:95], s51 offen
	s_mov_b32 s26, s86
	s_mov_b32 s86, s27
	s_mov_b32 s27, s32
	s_mov_b32 s32, s37
	s_cmp_eq_u32 s22, s23
	s_cbranch_scc1 .Lp6_B8done
	s_branch .Lp6c0_top
.Lp6_B8done:
	s_waitcnt vmcnt(0)
	v_lshl_add_u32 v1, v178, 2, s85
	ds_read_b32 v197, v1 offset:0
	ds_read_b32 v198, v1 offset:256
	ds_read_b32 v199, v1 offset:512
	ds_read_b32 v200, v1 offset:768
	ds_read_b32 v202, v1 offset:1024
	ds_read_b32 v203, v1 offset:1280
	ds_read_b32 v204, v1 offset:1536
	ds_read_b32 v205, v1 offset:1792
	ds_read_b32 v206, v1 offset:2048
	ds_read_b32 v207, v1 offset:2304
	ds_read_b32 v212, v1 offset:2560
	ds_read_b32 v213, v1 offset:2816
	ds_read_b32 v214, v1 offset:3072
	ds_read_b32 v221, v1 offset:3328
	s_waitcnt lgkmcnt(0)
	s_mov_b32 s2, 0
	s_mov_b64 s[6:7], -1
	s_or_b32 s96, s2, s33
	s_ashr_i32 s97, s96, 31
	v_and_b32_e32 v183, 64, v178
	s_mov_b32 s86, 0x19000
	s_branch .LBB0_975
